# LN1+router phase: LayerNorm weight/bias rows staged once per workgroup in spare LDS; per-group global reloads behind stores become ds_read_b128 (lgkmcnt waits), both layers
# baseline (speedup 1.0000x reference)
; #define GAS __attribute__((address_space(1)))
; template <bool X8>
; __device__ __forceinline__ void ln_router_phase(Frame& F, int layer) {
;     PHASE_ARGS();
;     const GAS bf16_t* R = (const GAS bf16_t*)(F.ws + WS_R); GAS bf16_t* X1B = (GAS bf16_t*)(F.ws + WS_X1B); GAS unsigned char* X1B8 = F.ws + WS_X1B8;
;     const GAS float* g1 = GIN(8) + (size_t)layer * D_MODEL; const GAS float* b1 = GIN(9) + (size_t)layer * D_MODEL;
;     const GAS float* wrt = GIN(10) + (size_t)layer * D_MODEL * N_EXPERTS; const GAS float* rbias = GIN(11) + (size_t)layer * N_EXPERTS;
;     GAS int* PE = (GAS int*)(F.ws + WS_PE); GAS int* PP = (GAS int*)(F.ws + WS_PP); GAS float* PG = (GAS float*)(F.ws + WS_PG); GAS int* RM = (GAS int*)(F.ws + WS_RM);
;     GAS unsigned* cnt = F.ctl + CW_CNT + layer * 64;
;     constexpr int XROW = 528, WROW = 144;
;     LAS unsigned char* XSb = F.lds; LAS unsigned char* WSb = F.lds + 64 * XROW; LAS float* PART = (LAS float*)F.lds; LAS float* LG = (LAS float*)(F.lds + 32768);
;     LAS int* LCNT = (LAS int*)(F.lds + 49152); LAS int* BASE = (LAS int*)(F.lds + 49408); LAS int* PEL = (LAS int*)(F.lds + 49664); LAS int* PLL = (LAS int*)(F.lds + 51712);
;     PHASE_IDS();
;     const int g = lane >> 4, i = lane & 15;
;     for (int bt = F.bid; bt < T / 64; bt += F.G) {
;         const int tok0 = bt * 64;
; #pragma unroll 1
;         for (int pr = 0; pr < 4; ++pr) {
;             f32x4 ys[2][4][2];
; #pragma unroll
;             for (int tt = 0; tt < 2; ++tt) { const size_t token = (size_t)(tok0 + 8 * w + 2 * pr + tt);
;                 const GAS u32x4* rp = (const GAS u32x4*)(R + token * D_MODEL) + lane;
; #pragma unroll
;                 for (int j = 0; j < 4; ++j) { const u32x4 r = rp[64 * j]; ys[tt][j][0] = (f32x4){bflo(r.x), bfhi(r.x), bflo(r.y), bfhi(r.y)}; ys[tt][j][1] = (f32x4){bflo(r.z), bfhi(r.z), bflo(r.w), bfhi(r.w)}; } }
; #pragma unroll
;             for (int tt = 0; tt < 2; ++tt) { const size_t token = (size_t)(tok0 + 8 * w + 2 * pr + tt); float s = 0.f;
; #pragma unroll
;                 for (int j = 0; j < 4; ++j)
; #pragma unroll
;                     for (int h = 0; h < 2; ++h) s += (ys[tt][j][h][0] + ys[tt][j][h][1]) + (ys[tt][j][h][2] + ys[tt][j][h][3]);
;                 const float mean = wave_sum(s) * (1.0f / D_MODEL); float s2 = 0.f;
; #pragma unroll
;                 for (int j = 0; j < 4; ++j)
; #pragma unroll
.LBB0_1303:
	s_cmp_lt_i32 s54, 8
	s_cselect_b64 s[58:59], -1, 0
	s_and_b64 s[0:1], s[58:59], s[4:5]
	s_andn2_b64 vcc, exec, s[0:1]
	s_cbranch_vccnz .LBB0_1327
	v_readlane_b32 s4, v254, 1
	v_readlane_b32 s0, v254, 0
	s_mov_b64 s[62:63], s[52:53]
	s_mov_b32 s1, s95
	s_mov_b32 s2, 0
	s_mov_b64 s[6:7], s[52:53]
	v_readlane_b32 s5, v254, 2
	s_waitcnt vmcnt(5)
	v_mov_b32_e32 v50, v0
	s_mov_b32 s61, 0
	s_cmpk_gt_i32 s0, 0xff
	v_readfirstlane_b32 s12, v50
	s_cbranch_scc1 .LBB0_1327
	v_mbcnt_lo_u32_b32 v2, -1, 0
	v_mbcnt_hi_u32_b32 v2, -1, v2
	v_and_b32_e32 v3, 64, v2
	v_add_u32_e32 v3, 64, v3
	v_xor_b32_e32 v6, 1, v2
	v_cmp_lt_i32_e32 vcc, v6, v3
	s_add_u32 s64, s62, 0x35300000
	s_addc_u32 s65, s63, 0
	v_cndmask_b32_e32 v6, v2, v6, vcc
	v_lshlrev_b32_e32 v53, 2, v6
	v_xor_b32_e32 v6, 2, v2
	v_cmp_lt_i32_e32 vcc, v6, v3
	s_add_u32 s66, s62, 0x35500000
	s_addc_u32 s67, s63, 0
	v_cndmask_b32_e32 v6, v2, v6, vcc
	v_lshlrev_b32_e32 v89, 2, v6
	v_xor_b32_e32 v6, 4, v2
	v_cmp_lt_i32_e32 vcc, v6, v3
	v_lshlrev_b32_e32 v7, 4, v50
	s_add_u32 s68, s62, 0x35600000
	v_cndmask_b32_e32 v6, v2, v6, vcc
	v_lshlrev_b32_e32 v166, 2, v6
	v_xor_b32_e32 v6, 8, v2
	v_cmp_lt_i32_e32 vcc, v6, v3
	s_waitcnt vmcnt(2)
	v_and_b32_e32 v54, 0x1f0, v7
	v_mov_b32_e32 v55, 0
	v_cndmask_b32_e32 v6, v2, v6, vcc
	v_lshlrev_b32_e32 v167, 2, v6
	v_xor_b32_e32 v6, 16, v2
	v_cmp_lt_i32_e32 vcc, v6, v3
	s_load_dwordx4 s[8:11], s[4:5], 0x40
	s_load_dwordx2 s[14:15], s[4:5], 0x58
	v_cndmask_b32_e32 v6, v2, v6, vcc
	v_lshlrev_b32_e32 v168, 2, v6
	v_xor_b32_e32 v6, 32, v2
	v_cmp_lt_i32_e32 vcc, v6, v3
	s_addc_u32 s69, s63, 0
	s_ashr_i32 s13, s12, 6
	v_cndmask_b32_e32 v2, v2, v6, vcc
	v_lshlrev_b32_e32 v169, 2, v2
	v_lshl_add_u64 v[2:3], s[62:63], 0, v[54:55]
	s_mov_b64 s[4:5], 0x31300000
	v_lshl_add_u64 v[56:57], v[2:3], 0, s[4:5]
	s_lshl_b32 s4, s13, 4
	v_and_b32_e32 v4, 15, v50
	s_and_b32 s4, s4, 48
	v_bfe_u32 v5, v50, 4, 2
	v_and_b32_e32 v2, 0x70, v7
	v_or_b32_e32 v7, s4, v4
	s_movk_i32 s17, 0x210
	v_mov_b32_e32 v8, s2
	v_and_b32_e32 v1, 63, v50
	s_ashr_i32 s12, s12, 8
	v_mad_u32_u24 v20, v7, s17, v8
	v_lshlrev_b32_e32 v7, 3, v5
	v_lshlrev_b32_e32 v5, 2, v5
	v_add_u32_e32 v18, s2, v54
	v_lshl_or_b32 v5, s12, 6, v5
	v_ashrrev_i32_e32 v51, 31, v50
	v_lshlrev_b32_e32 v54, 2, v1
	v_and_b32_e32 v27, 7, v50
	v_lshlrev_b32_e32 v6, 3, v50
	v_or_b32_e32 v24, s4, v5
	v_lshl_add_u32 v25, v4, 2, s2
	v_add_u32_e32 v172, s2, v54
	s_waitcnt lgkmcnt(0)
	v_lshl_add_u64 v[58:59], s[14:15], 0, v[54:55]
	v_lshl_add_u64 v[4:5], v[50:51], 2, s[6:7]
	s_mov_b64 s[70:71], 0x1000
	v_lshlrev_b32_e32 v54, 2, v27
	s_add_i32 s16, s2, 0x8400
	v_bfe_u32 v3, v50, 2, 2
	v_lshl_or_b32 v21, s12, 7, v7
	v_and_b32_e32 v6, 24, v6
	s_waitcnt vmcnt(0)
	v_lshl_add_u64 v[62:63], v[4:5], 0, s[70:71]
	v_lshl_add_u64 v[4:5], s[62:63], 0, v[54:55]
	s_mov_b64 s[6:7], 0x35400000
	v_add_u32_e32 v22, s16, v6
	v_ashrrev_i32_e32 v64, 3, v50
	v_lshl_add_u64 v[66:67], v[4:5], 0, s[6:7]
	v_lshlrev_b32_e32 v54, 5, v1
	s_movk_i32 s6, 0x90
	v_or_b32_e32 v31, v21, v3
	v_add_u32_e32 v23, 0x240, v22
	v_or_b32_e32 v4, 0x1000, v54
	v_mov_b32_e32 v5, v55
	v_ashrrev_i32_e32 v65, 31, v64
	v_mul_lo_u32 v31, v31, s6
	v_lshl_add_u64 v[72:73], s[8:9], 0, v[4:5]
	v_lshl_add_u64 v[74:75], s[10:11], 0, v[4:5]
	v_lshlrev_b64 v[4:5], 7, v[64:65]
	v_add_u32_e32 v65, v31, v22
	v_add_u32_e32 v177, v31, v23
	v_or_b32_e32 v31, 32, v21
	v_lshlrev_b32_e32 v32, 1, v31
	v_or_b32_e32 v31, v31, v3
	v_mul_lo_u32 v31, v31, s6
	v_lshlrev_b32_e32 v30, 1, v21
	v_add_u32_e32 v178, v31, v22
	v_add_u32_e32 v179, v31, v23
	v_or_b32_e32 v31, 64, v21
	v_or_b32_e32 v21, 0x60, v21
	v_lshlrev_b32_e32 v33, 1, v31
	v_or_b32_e32 v31, v31, v3
	v_or_b32_e32 v3, v21, v3
	v_add_u32_e32 v6, 0x200, v50
	v_add_u32_e32 v10, 0x400, v50
	v_add_u32_e32 v14, 0x600, v50
	v_mul_lo_u32 v3, v3, s6
	v_ashrrev_i32_e32 v174, 5, v6
	v_ashrrev_i32_e32 v175, 5, v10
	v_ashrrev_i32_e32 v176, 5, v14
	v_ashrrev_i32_e32 v6, 3, v6
	v_ashrrev_i32_e32 v10, 3, v10
	v_ashrrev_i32_e32 v14, 3, v14
	v_add_u32_e32 v182, v3, v22
	v_add_u32_e32 v183, v3, v23
	v_mov_b32_e32 v3, v55
	v_add_u32_e32 v19, s2, v2
	v_ashrrev_i32_e32 v7, 31, v6
	v_ashrrev_i32_e32 v11, 31, v10
	v_ashrrev_i32_e32 v15, 31, v14
	v_lshl_add_u64 v[2:3], s[62:63], 0, v[2:3]
	s_mov_b64 s[20:21], 0x1d210000
	v_lshlrev_b64 v[8:9], 7, v[6:7]
	v_lshlrev_b64 v[12:13], 7, v[10:11]
	v_lshlrev_b64 v[16:17], 7, v[14:15]
	v_lshl_add_u64 v[2:3], v[2:3], 0, s[20:21]
	s_lshl_b32 s3, s13, 3
	v_ashrrev_i32_e32 v173, 5, v50
	v_mul_lo_u32 v31, v31, s6
	v_lshl_add_u64 v[80:81], v[2:3], 0, v[4:5]
	v_lshl_add_u64 v[82:83], v[2:3], 0, v[8:9]
	v_lshl_add_u64 v[84:85], v[2:3], 0, v[12:13]
	v_lshl_add_u64 v[86:87], v[2:3], 0, v[16:17]
	s_lshl_b32 s22, s0, 6
	v_lshlrev_b32_e32 v2, 4, v27
	v_and_b32_e32 v26, 56, v50
	s_mov_b64 s[12:13], 0xff
	v_lshl_add_u64 v[68:69], s[8:9], 0, v[54:55]
	v_lshl_add_u64 v[70:71], s[10:11], 0, v[54:55]
	v_lshlrev_b32_e32 v252, 4, v50
	v_mov_b32_e32 v253, 0
	v_lshl_add_u64 v[244:245], s[8:9], 0, v[252:253]
	v_lshl_add_u64 v[252:253], s[10:11], 0, v[252:253]
	global_load_dwordx4 v[244:247], v[244:245], off
	global_load_dwordx4 v[248:251], v[252:253], off
	v_lshrrev_b32_e32 v255, 7, v50
	v_lshlrev_b32_e32 v255, 11, v255
	v_and_b32_e32 v240, 1, v50
	v_lshl_or_b32 v255, v240, 10, v255
	v_bfe_u32 v240, v50, 1, 6
	v_lshl_or_b32 v255, v240, 4, v255
	v_add_u32_e32 v255, 0x14000, v255
	v_mbcnt_lo_u32_b32 v240, -1, 0
	v_mbcnt_hi_u32_b32 v240, -1, v240
	v_lshlrev_b32_e32 v240, 4, v240
	v_add_u32_e32 v240, 0x14000, v240
	s_waitcnt vmcnt(0)
	ds_write_b128 v255, v[244:247]
	ds_write_b128 v255, v[248:251] offset:8192
	s_waitcnt lgkmcnt(0)
	s_barrier
; #define GAS __attribute__((address_space(1)))
; template <bool X8>
; __device__ __forceinline__ void ln_router_phase(Frame& F, int layer) {
;     ...
;         const int tt4 = w & 3, kh = w >> 2;
;         u32x4 xr[4], wq[4];
;         const GAS bf16_t* wrb = (const GAS bf16_t*)(F.ws + WS_WRB) + (size_t)layer * D_MODEL * N_EXPERTS;
; #pragma unroll
;         for (int j = 0; j < 4; ++j) { const int idx = tid + 512 * j, row = idx >> 5, c8 = idx & 31; xr[j] = *(const GAS u32x4*)(X1B + (size_t)(tok0 + row) * D_MODEL + 8 * c8); }
; #pragma unroll
;         for (int j = 0; j < 4; ++j) { const int idx = tid + 512 * j, row = idx >> 3, c8 = idx & 7; wq[j] = *(const GAS u32x4*)(wrb + (size_t)row * N_EXPERTS + 8 * c8); }
; #pragma unroll 1
;         for (int ke = 0; ke < 8; ++ke) { const int k1 = 256 * (ke + 1);
; #pragma unroll
;             for (int j = 0; j < 4; ++j) { const int idx = tid + 512 * j, row = idx >> 5, c8 = idx & 31; *(LAS u32x4*)(XSb + row * XROW + c8 * 16) = xr[j]; }
; #pragma unroll
;             for (int j = 0; j < 4; ++j) { const int idx = tid + 512 * j, row = idx >> 3, c8 = idx & 7; *(LAS u32x4*)(WSb + row * WROW + c8 * 16) = wq[j]; }
;             LDS_BARRIER();
;             if (ke < 7) {
; #pragma unroll
;                 for (int j = 0; j < 4; ++j) { const int idx = tid + 512 * j, row = idx >> 5, c8 = idx & 31; xr[j] = *(const GAS u32x4*)(X1B + (size_t)(tok0 + row) * D_MODEL + k1 + 8 * c8); }
; #pragma unroll
;                 for (int j = 0; j < 4; ++j) { const int idx = tid + 512 * j, row = idx >> 3, c8 = idx & 7; wq[j] = *(const GAS u32x4*)(wrb + (size_t)(k1 + row) * N_EXPERTS + 8 * c8); }
;             }
;             { const unsigned wsb = (unsigned)(size_t)WSb; const int q = i >> 2, p4 = i & 3;
; #pragma unroll
;               for (int ks = 0; ks < 4; ++ks) { const int kk0 = 128 * kh + 32 * ks;
;                 const bf16x8 a = *(const LAS bf16x8*)(XSb + (tt4 * 16 + i) * XROW + (kk0 + 8 * g) * 2);
;                 s16x4 lo4[4], hi4[4];
;                 tr_read4x2<32>(lo4, hi4, wsb + (kk0 + 8 * g + q) * WROW + 8 * p4, wsb + (kk0 + 8 * g + 4 + q) * WROW + 8 * p4);
; #pragma unroll
;                 for (int nb = 0; nb < 4; ++nb) dacc[nb] = mfma16(a, TRCAT(lo4[nb], hi4[nb]), dacc[nb]); } }
;             LDS_BARRIER();
;         }
; #pragma unroll
;         for (int nb = 0; nb < 4; ++nb)
; #pragma unroll
	v_or_b32_e32 v54, 0x1800, v54
	v_mul_lo_u32 v7, v173, s17
	v_mul_lo_u32 v11, v174, s17
	v_mul_lo_u32 v15, v175, s17
	v_mul_lo_u32 v28, v176, s17
	v_mul_lo_u32 v29, v64, s6
	v_mul_lo_u32 v6, v6, s6
	v_mul_lo_u32 v10, v10, s6
	v_mul_lo_u32 v14, v14, s6
	v_add_u32_e32 v180, v31, v22
	v_add_u32_e32 v181, v31, v23
	v_lshlrev_b32_e32 v31, 1, v21
	v_lshlrev_b32_e32 v21, 8, v24
	s_add_i32 s72, s22, s3
	v_or_b32_e32 v16, v16, v2
	s_mov_b64 s[20:21], 0x1d218000
	v_or_b32_e32 v12, v12, v2
	v_or_b32_e32 v8, v8, v2
	v_or_b32_e32 v4, v4, v2
	v_and_b32_e32 v2, 31, v50
	v_mov_b32_e32 v3, 0x31300200
	v_lshlrev_b32_e32 v52, 3, v1
	v_lshl_add_u32 v170, v50, 5, s2
	v_cmp_gt_i32_e64 s[4:5], 64, v50
	v_lshl_add_u32 v171, v50, 2, s2
	v_lshlrev_b64 v[60:61], v26, s[12:13]
	v_lshl_add_u64 v[76:77], s[8:9], 0, v[54:55]
	v_lshl_add_u64 v[78:79], s[10:11], 0, v[54:55]
	v_cmp_lt_u32_e64 s[6:7], 7, v1
	v_cmp_lt_u32_e64 s[8:9], 15, v1
	v_cmp_lt_u32_e64 s[10:11], 23, v1
	v_cmp_lt_u32_e64 s[12:13], 31, v1
	v_cmp_lt_u32_e64 s[14:15], 39, v1
	v_cmp_lt_u32_e64 s[16:17], 47, v1
	v_cmp_eq_u32_e64 s[18:19], 56, v26
	s_or_b32 s74, s72, 1
	s_lshl_b32 s24, s1, 6
	v_lshlrev_b32_e32 v88, 4, v1
	v_lshl_add_u64 v[90:91], v[16:17], 0, s[20:21]
	v_lshl_add_u64 v[92:93], v[12:13], 0, s[20:21]
	v_lshl_add_u64 v[94:95], v[8:9], 0, s[20:21]
	v_lshl_add_u64 v[96:97], v[4:5], 0, s[20:21]
	v_lshl_or_b32 v54, v2, 4, v3
	v_add_u32_e32 v98, s22, v176
	v_add_u32_e32 v100, s22, v175
	v_add_u32_e32 v102, s22, v174
	v_add_u32_e32 v104, s22, v173
	s_mov_b32 s25, 0x1d300000
	v_mov_b32_e32 v184, 0x3727c5ac
	s_mov_b32 s33, 0x800000
	s_mov_b32 s50, 0x31300000
	s_mov_b32 s51, 0x71f00000
	s_mov_b64 s[76:77], 0x2000
	v_add_u32_e32 v185, v18, v7
	v_add_u32_e32 v186, v18, v11
	v_add_u32_e32 v187, v18, v15
	v_add_u32_e32 v188, v18, v28
	v_add_u32_e32 v189, v19, v29
	v_add_u32_e32 v190, v19, v6
	v_add_u32_e32 v191, v19, v10
	v_add_u32_e32 v192, v19, v14
	v_add_u32_e32 v193, v20, v30
	v_add_u32_e32 v194, v20, v32
	v_add_u32_e32 v195, v20, v33
	v_add_u32_e32 v196, v20, v31
	s_mov_b64 s[78:79], 0x8000
	s_mov_b64 s[80:81], 0x200
	v_add_u32_e32 v197, v25, v21
	s_mov_b32 s56, 0xbfb8aa3b
	s_mov_b32 s57, 0x42ce8ed0
	s_mov_b32 s84, 0xc2b17218
	v_mov_b32_e32 v198, 1
	v_mov_b32_e32 v199, 0x7f800000
	v_mov_b32_e32 v200, 0xff800000
	s_branch .LBB0_1307

; #define GAS __attribute__((address_space(1)))
; template <bool X8>
; __device__ __forceinline__ void ln_router_phase(Frame& F, int layer) {
;     ...
;         for (int pr = 0; pr < 4; ++pr) {
;             f32x4 ys[2][4][2];
; #pragma unroll
;             for (int tt = 0; tt < 2; ++tt) { const size_t token = (size_t)(tok0 + 8 * w + 2 * pr + tt);
;                 const GAS u32x4* rp = (const GAS u32x4*)(R + token * D_MODEL) + lane;
; #pragma unroll
;                 for (int j = 0; j < 4; ++j) { const u32x4 r = rp[64 * j]; ys[tt][j][0] = (f32x4){bflo(r.x), bfhi(r.x), bflo(r.y), bfhi(r.y)}; ys[tt][j][1] = (f32x4){bflo(r.z), bfhi(r.z), bflo(r.w), bfhi(r.w)}; } }
; #pragma unroll
;             for (int tt = 0; tt < 2; ++tt) { const size_t token = (size_t)(tok0 + 8 * w + 2 * pr + tt); float s = 0.f;
; #pragma unroll
;                 for (int j = 0; j < 4; ++j)
; #pragma unroll
;                     for (int h = 0; h < 2; ++h) s += (ys[tt][j][h][0] + ys[tt][j][h][1]) + (ys[tt][j][h][2] + ys[tt][j][h][3]);
;                 const float mean = wave_sum(s) * (1.0f / D_MODEL); float s2 = 0.f;
.LBB0_1308:
	v_lshl_add_u64 v[26:27], s[62:63], 0, v[24:25]
	v_lshl_add_u64 v[28:29], s[62:63], 0, v[20:21]
	v_add_co_u32_e32 v46, vcc, 0x1d300000, v26
	v_add_co_u32_e64 v48, s[20:21], s25, v28
	s_nop 0
	v_addc_co_u32_e32 v47, vcc, 0, v27, vcc
	v_addc_co_u32_e64 v49, s[20:21], 0, v29, s[20:21]
	ds_read_b128 v[2:5], v240 offset:1024
	ds_read_b128 v[10:13], v240 offset:0
	ds_read_b128 v[6:9], v240 offset:9216
	ds_read_b128 v[14:17], v240 offset:8192
	global_load_dwordx4 v[128:131], v[48:49], off offset:1024
	global_load_dwordx4 v[132:135], v[48:49], off offset:2048
	global_load_dwordx4 v[42:45], v[48:49], off offset:3072
	global_load_dwordx4 v[136:139], v[48:49], off
	global_load_dwordx4 v[202:205], v[46:47], off offset:1024
	global_load_dwordx4 v[206:209], v[46:47], off offset:2048
	global_load_dwordx4 v[210:213], v[46:47], off offset:3072
	global_load_dwordx4 v[214:217], v[46:47], off
	v_add_co_u32_e64 v126, s[20:21], s50, v26
	v_lshl_add_u64 v[38:39], s[62:63], 0, v[22:23]
	s_nop 0
	v_addc_co_u32_e64 v127, s[20:21], 0, v27, s[20:21]
	v_add_co_u32_e64 v124, s[20:21], s51, v38
	v_lshl_add_u64 v[40:41], s[62:63], 0, v[18:19]
	s_nop 0
	v_addc_co_u32_e64 v125, s[20:21], 0, v39, s[20:21]
	v_add_co_u32_e64 v28, s[20:21], s50, v28
	v_mov_b32_e32 v32, 0
	s_nop 0
	v_addc_co_u32_e64 v29, s[20:21], 0, v29, s[20:21]
	v_add_co_u32_e64 v38, s[20:21], s51, v40
	v_mov_b32_e32 v33, 0
	s_nop 0
	v_addc_co_u32_e64 v39, s[20:21], 0, v41, s[20:21]
	v_mov_b32_e32 v36, 0
	v_mov_b32_e32 v37, 0
	v_mov_b32_e32 v34, 0
	v_mov_b32_e32 v35, 0
	v_mov_b32_e32 v30, 0
	v_mov_b32_e32 v31, 0
	v_mov_b32_e32 v120, 0
	v_mov_b32_e32 v121, 0
	s_add_i32 s22, s22, -1
	v_lshl_add_u64 v[18:19], v[18:19], 0, s[70:71]
	v_lshl_add_u64 v[20:21], v[20:21], 0, s[76:77]
	v_lshl_add_u64 v[22:23], v[22:23], 0, s[70:71]
	v_lshl_add_u64 v[24:25], v[24:25], 0, s[76:77]
	s_cmp_eq_u32 s22, 0
	s_waitcnt vmcnt(7)
	v_lshlrev_b32_e32 v116, 16, v130
	v_and_b32_e32 v117, 0xffff0000, v130
	v_lshlrev_b32_e32 v118, 16, v131
	v_and_b32_e32 v119, 0xffff0000, v131
	s_waitcnt vmcnt(6)
	v_lshlrev_b32_e32 v106, 16, v132
	v_and_b32_e32 v110, 0xffff0000, v132
	s_waitcnt vmcnt(4)
	v_lshlrev_b32_e32 v155, 16, v136
	v_lshlrev_b32_e32 v154, 16, v138
	v_and_b32_e32 v153, 0xffff0000, v136
	v_and_b32_e32 v152, 0xffff0000, v138
	v_lshlrev_b32_e32 v123, 16, v129
	v_lshlrev_b32_e32 v122, 16, v128
	v_and_b32_e32 v147, 0xffff0000, v129
	v_and_b32_e32 v146, 0xffff0000, v128
	v_lshlrev_b32_e32 v114, 16, v134
	v_and_b32_e32 v142, 0xffff0000, v134
	s_waitcnt vmcnt(3)
	v_lshlrev_b32_e32 v162, 16, v204
	v_and_b32_e32 v163, 0xffff0000, v204
	v_lshlrev_b32_e32 v164, 16, v205
	v_and_b32_e32 v165, 0xffff0000, v205
	s_waitcnt vmcnt(2)
	v_lshlrev_b32_e32 v148, 16, v206
	v_and_b32_e32 v156, 0xffff0000, v206
	v_lshlrev_b32_e32 v150, 16, v207
	v_and_b32_e32 v158, 0xffff0000, v207
	s_waitcnt vmcnt(1)
	v_lshlrev_b32_e32 v128, 16, v210
	v_and_b32_e32 v129, 0xffff0000, v210
	v_lshlrev_b32_e32 v130, 16, v211
	v_and_b32_e32 v131, 0xffff0000, v211
	v_lshlrev_b32_e32 v132, 16, v212
	v_and_b32_e32 v136, 0xffff0000, v212
	v_lshlrev_b32_e32 v134, 16, v213
	v_and_b32_e32 v138, 0xffff0000, v213
	s_waitcnt vmcnt(0) lgkmcnt(0)
	v_lshlrev_b32_e32 v205, 16, v214
	v_lshlrev_b32_e32 v204, 16, v216
	v_and_b32_e32 v207, 0xffff0000, v214
	v_and_b32_e32 v206, 0xffff0000, v216
	v_lshlrev_b32_e32 v211, 16, v215
	v_lshlrev_b32_e32 v210, 16, v217
	v_and_b32_e32 v213, 0xffff0000, v215
	v_and_b32_e32 v212, 0xffff0000, v217
	v_lshlrev_b32_e32 v26, 16, v42
	v_and_b32_e32 v27, 0xffff0000, v42
	v_lshlrev_b32_e32 v40, 16, v43
	v_and_b32_e32 v41, 0xffff0000, v43
	v_lshlrev_b32_e32 v215, 16, v203
	v_lshlrev_b32_e32 v214, 16, v202
	v_and_b32_e32 v203, 0xffff0000, v203
	v_and_b32_e32 v202, 0xffff0000, v202
	v_pk_add_f32 v[224:225], v[204:205], v[206:207]
	v_pk_add_f32 v[226:227], v[210:211], v[212:213]
	v_lshlrev_b32_e32 v42, 16, v44
	v_and_b32_e32 v46, 0xffff0000, v44
	v_lshlrev_b32_e32 v145, 16, v137
	v_lshlrev_b32_e32 v144, 16, v139
	v_and_b32_e32 v141, 0xffff0000, v137
	v_and_b32_e32 v140, 0xffff0000, v139
	v_add_f32_e32 v43, v26, v27
	v_add_f32_e32 v47, v40, v41
	v_pk_add_f32 v[228:229], v[214:215], v[202:203]
	v_pk_add_f32 v[224:225], v[224:225], v[226:227]
	v_pk_add_f32 v[216:217], v[154:155], v[152:153]
	v_pk_add_f32 v[218:219], v[144:145], v[140:141]
	v_pk_add_f32 v[220:221], v[122:123], v[146:147]
	v_pk_add_f32 v[232:233], v[42:43], v[46:47]
	v_pk_add_f32 v[226:227], v[228:229], v[228:229] op_sel_hi:[0,1]
	v_add_f32_e32 v47, 0, v225
	v_add_f32_e32 v149, v162, v163
	v_add_f32_e32 v157, v164, v165
	v_pk_add_f32 v[216:217], v[216:217], v[218:219]
	v_pk_add_f32 v[218:219], v[220:221], v[220:221] op_sel_hi:[0,1]
	v_mov_b32_e32 v151, v227
	v_add_f32_e32 v159, v224, v47
	v_lshlrev_b32_e32 v161, 16, v209
	v_lshlrev_b32_e32 v160, 16, v208
	v_and_b32_e32 v209, 0xffff0000, v209
	v_and_b32_e32 v208, 0xffff0000, v208
	v_pk_add_f32 v[228:229], v[148:149], v[156:157]
	v_add_f32_e32 v43, 0, v217
	v_mov_b32_e32 v109, v219
	v_pk_add_f32 v[218:219], v[150:151], v[158:159]
	v_lshlrev_b32_e32 v108, 16, v133
	v_and_b32_e32 v112, 0xffff0000, v133
	v_add_f32_e32 v107, v116, v117
	v_add_f32_e32 v111, v118, v119
	v_pk_add_f32 v[230:231], v[160:161], v[208:209]
	v_add_f32_e32 v113, v216, v43
	v_pk_add_f32 v[218:219], v[228:229], v[218:219]
	v_lshlrev_b32_e32 v115, 16, v135
	v_and_b32_e32 v143, 0xffff0000, v135
	v_pk_add_f32 v[220:221], v[106:107], v[110:111]
	v_pk_add_f32 v[230:231], v[230:231], v[230:231] op_sel_hi:[0,1]
	v_pk_add_f32 v[216:217], v[108:109], v[112:113]
	v_pk_add_f32 v[218:219], v[218:219], v[218:219] op_sel_hi:[0,1]
	v_pk_add_f32 v[222:223], v[114:115], v[142:143]
	v_add_f32_e32 v133, v128, v129
	v_add_f32_e32 v137, v130, v131
	v_mov_b32_e32 v135, v231
	v_pk_add_f32 v[216:217], v[220:221], v[216:217]
	v_mov_b32_e32 v139, v219
	v_pk_add_f32 v[222:223], v[222:223], v[222:223] op_sel_hi:[0,1]
	v_pk_add_f32 v[234:235], v[132:133], v[136:137]
	v_pk_add_f32 v[216:217], v[216:217], v[216:217] op_sel_hi:[0,1]
	v_pk_add_f32 v[218:219], v[134:135], v[138:139]
	v_lshlrev_b32_e32 v44, 16, v45
	v_and_b32_e32 v48, 0xffff0000, v45
	v_mov_b32_e32 v45, v223
	v_mov_b32_e32 v49, v217
	v_pk_add_f32 v[218:219], v[234:235], v[218:219]
	v_pk_add_f32 v[216:217], v[44:45], v[48:49]
	v_add_f32_e32 v45, v218, v219
	ds_bpermute_b32 v49, v53, v45
	v_pk_add_f32 v[216:217], v[232:233], v[216:217]
	s_waitcnt lgkmcnt(0)
; __device__ __forceinline__ float wave_sum(float v) {
; #pragma unroll
;     for (int o = 1; o < 64; o <<= 1) v += __shfl_xor(v, o);
;     return v;
; }
; template <bool X8>
; __device__ __forceinline__ void ln_router_phase(Frame& F, int layer) {
;     ...
;             for (int tt = 0; tt < 2; ++tt) { const size_t token = (size_t)(tok0 + 8 * w + 2 * pr + tt); float s = 0.f;
; #pragma unroll
;                 for (int j = 0; j < 4; ++j)
; #pragma unroll
;                     for (int h = 0; h < 2; ++h) s += (ys[tt][j][h][0] + ys[tt][j][h][1]) + (ys[tt][j][h][2] + ys[tt][j][h][3]);
;                 const float mean = wave_sum(s) * (1.0f / D_MODEL); float s2 = 0.f;
; #pragma unroll
;                 for (int j = 0; j < 4; ++j)
; #pragma unroll
;                     for (int h = 0; h < 2; ++h) { ys[tt][j][h] = ys[tt][j][h] - mean; s2 += (ys[tt][j][h][0] * ys[tt][j][h][0] + ys[tt][j][h][1] * ys[tt][j][h][1]) + (ys[tt][j][h][2] * ys[tt][j][h][2] + ys[tt][j][h][3] * ys[tt][j][h][3]); }
;                 const float rstd = rsqrtf(wave_sum(s2) * (1.0f / D_MODEL) + LN_EPS);
	v_add_f32_e32 v45, v45, v49
	ds_bpermute_b32 v49, v89, v45
	v_add_f32_e32 v43, v216, v217
	ds_bpermute_b32 v47, v53, v43
	s_waitcnt lgkmcnt(1)
	v_add_f32_e32 v45, v45, v49
	ds_bpermute_b32 v49, v166, v45
	s_waitcnt lgkmcnt(1)
	v_add_f32_e32 v43, v43, v47
	ds_bpermute_b32 v47, v89, v43
	s_waitcnt lgkmcnt(1)
	v_add_f32_e32 v45, v45, v49
	ds_bpermute_b32 v49, v167, v45
	s_waitcnt lgkmcnt(1)
	v_add_f32_e32 v43, v43, v47
	ds_bpermute_b32 v47, v166, v43
	s_waitcnt lgkmcnt(1)
	v_add_f32_e32 v45, v45, v49
	ds_bpermute_b32 v49, v168, v45
	s_waitcnt lgkmcnt(1)
	v_add_f32_e32 v43, v43, v47
	ds_bpermute_b32 v47, v167, v43
	s_waitcnt lgkmcnt(1)
	v_add_f32_e32 v45, v45, v49
	ds_bpermute_b32 v49, v169, v45
	s_waitcnt lgkmcnt(1)
	v_add_f32_e32 v43, v43, v47
	ds_bpermute_b32 v47, v168, v43
	s_waitcnt lgkmcnt(1)
	v_add_f32_e32 v45, v45, v49
	v_fmac_f32_e32 v213, 0xba000000, v45
	v_fmac_f32_e32 v211, 0xba000000, v45
	v_fmac_f32_e32 v207, 0xba000000, v45
	v_fmac_f32_e32 v205, 0xba000000, v45
	v_fmac_f32_e32 v212, 0xba000000, v45
	v_fmac_f32_e32 v210, 0xba000000, v45
	v_fmac_f32_e32 v206, 0xba000000, v45
	v_fmac_f32_e32 v204, 0xba000000, v45
	v_fmac_f32_e32 v202, 0xba000000, v45
	v_fmac_f32_e32 v203, 0xba000000, v45
	v_fmac_f32_e32 v215, 0xba000000, v45
	v_fmac_f32_e32 v214, 0xba000000, v45
	v_mov_b32_e32 v216, v204
	v_mov_b32_e32 v217, v206
	v_mov_b32_e32 v218, v205
	v_mov_b32_e32 v219, v207
	v_mov_b32_e32 v220, v205
	v_mov_b32_e32 v221, v204
	v_mov_b32_e32 v204, v207
	v_mov_b32_e32 v205, v206
	v_mov_b32_e32 v206, v210
	v_mov_b32_e32 v207, v212
	v_mov_b32_e32 v222, v211
	v_mov_b32_e32 v223, v213
	v_mov_b32_e32 v224, v211
	v_mov_b32_e32 v225, v210
	v_mov_b32_e32 v210, v213
	v_mov_b32_e32 v211, v212
	v_mov_b32_e32 v212, v215
	v_mov_b32_e32 v213, v203
	v_mov_b32_e32 v215, v202
	v_pk_mul_f32 v[204:205], v[204:205], v[204:205]
	v_pk_mul_f32 v[210:211], v[210:211], v[210:211]
	v_pk_mul_f32 v[232:233], v[212:213], v[212:213]
	v_pk_mul_f32 v[234:235], v[214:215], v[214:215]
	v_fmac_f32_e32 v162, 0xba000000, v45
	v_fmac_f32_e32 v164, 0xba000000, v45
	v_pk_fma_f32 v[204:205], v[220:221], v[220:221], v[204:205]
	v_pk_fma_f32 v[210:211], v[224:225], v[224:225], v[210:211]
	v_pk_mov_b32 v[220:221], v[234:235], v[232:233] op_sel:[1,0]
	v_mov_b32_e32 v235, v233
	v_fmac_f32_e32 v163, 0xba000000, v45
	v_fmac_f32_e32 v165, 0xba000000, v45
	v_fmac_f32_e32 v208, 0xba000000, v45
	v_fmac_f32_e32 v209, 0xba000000, v45
	v_fmac_f32_e32 v161, 0xba000000, v45
	v_mul_f32_e32 v202, v162, v162
	v_mul_f32_e32 v226, v164, v164
	v_pk_add_f32 v[204:205], v[204:205], v[210:211]
	v_pk_add_f32 v[210:211], v[220:221], v[234:235]
	v_fmac_f32_e32 v158, 0xba000000, v45
	v_fmac_f32_e32 v150, 0xba000000, v45
	v_fmac_f32_e32 v156, 0xba000000, v45
	v_fmac_f32_e32 v148, 0xba000000, v45
	v_fmac_f32_e32 v160, 0xba000000, v45
	v_mov_b32_e32 v228, v161
	v_mov_b32_e32 v229, v209
	v_mov_b32_e32 v161, v208
	v_pk_fma_f32 v[202:203], v[162:163], v[162:163], v[202:203] op_sel_hi:[1,1,0]
	v_pk_fma_f32 v[226:227], v[164:165], v[164:165], v[226:227] op_sel_hi:[1,1,0]
	v_pk_add_f32 v[204:205], v[204:205], v[204:205] op_sel_hi:[0,1]
	v_pk_add_f32 v[210:211], v[210:211], v[210:211] op_sel_hi:[0,1]
	v_pk_mul_f32 v[236:237], v[228:229], v[228:229]
	v_pk_mul_f32 v[238:239], v[160:161], v[160:161]
	v_mul_f32_e32 v202, v148, v148
	v_mul_f32_e32 v226, v156, v156
	v_mul_f32_e32 v210, v150, v150
	v_mul_f32_e32 v204, v158, v158
	v_fmac_f32_e32 v128, 0xba000000, v45
	v_fmac_f32_e32 v130, 0xba000000, v45
	v_pk_mov_b32 v[224:225], v[238:239], v[236:237] op_sel:[1,0]
	v_mov_b32_e32 v239, v237
	v_pk_add_f32 v[202:203], v[202:203], v[226:227]
	v_pk_add_f32 v[204:205], v[210:211], v[204:205]
	s_waitcnt lgkmcnt(0)
	v_add_f32_e32 v43, v43, v47
	v_fmac_f32_e32 v129, 0xba000000, v45
	v_fmac_f32_e32 v131, 0xba000000, v45
	v_mul_f32_e32 v208, v128, v128
	v_mul_f32_e32 v230, v130, v130
	v_pk_add_f32 v[220:221], v[224:225], v[238:239]
	v_pk_add_f32 v[202:203], v[202:203], v[204:205]
	ds_bpermute_b32 v47, v169, v43
	v_fmac_f32_e32 v138, 0xba000000, v45
	v_fmac_f32_e32 v134, 0xba000000, v45
	v_fmac_f32_e32 v136, 0xba000000, v45
	v_fmac_f32_e32 v132, 0xba000000, v45
	v_pk_fma_f32 v[208:209], v[128:129], v[128:129], v[208:209] op_sel_hi:[1,1,0]
	v_pk_fma_f32 v[230:231], v[130:131], v[130:131], v[230:231] op_sel_hi:[1,1,0]
	v_pk_add_f32 v[220:221], v[220:221], v[220:221] op_sel_hi:[0,1]
	v_pk_add_f32 v[202:203], v[202:203], v[202:203] op_sel_hi:[0,1]
	v_mul_f32_e32 v208, v132, v132
	v_mul_f32_e32 v230, v136, v136
	v_mul_f32_e32 v220, v134, v134
	v_mul_f32_e32 v202, v138, v138
	v_pk_add_f32 v[208:209], v[208:209], v[230:231]
	v_pk_add_f32 v[202:203], v[220:221], v[202:203]
	s_waitcnt lgkmcnt(0)
	v_add_f32_e32 v43, v43, v47
	v_pk_add_f32 v[202:203], v[208:209], v[202:203]
	v_mov_b32_e32 v149, v156
	v_add_f32_e32 v45, v202, v203
	ds_bpermute_b32 v47, v53, v45
	v_mov_b32_e32 v151, v158
	v_mov_b32_e32 v133, v136
	v_mov_b32_e32 v135, v138
	v_fmac_f32_e32 v141, 0xba000000, v43
	s_waitcnt lgkmcnt(0)
	v_add_f32_e32 v45, v45, v47
	ds_bpermute_b32 v47, v89, v45
	v_fmac_f32_e32 v145, 0xba000000, v43
	v_fmac_f32_e32 v153, 0xba000000, v43
	v_fmac_f32_e32 v155, 0xba000000, v43
	v_fmac_f32_e32 v140, 0xba000000, v43
	s_waitcnt lgkmcnt(0)
	v_add_f32_e32 v45, v45, v47
	ds_bpermute_b32 v47, v166, v45
	v_fmac_f32_e32 v144, 0xba000000, v43
	v_fmac_f32_e32 v152, 0xba000000, v43
	v_fmac_f32_e32 v154, 0xba000000, v43
	v_fmac_f32_e32 v146, 0xba000000, v43
	s_waitcnt lgkmcnt(0)
	v_add_f32_e32 v45, v45, v47
	ds_bpermute_b32 v47, v167, v45
	v_fmac_f32_e32 v147, 0xba000000, v43
	v_fmac_f32_e32 v123, 0xba000000, v43
	v_fmac_f32_e32 v122, 0xba000000, v43
	v_fmac_f32_e32 v116, 0xba000000, v43
	s_waitcnt lgkmcnt(0)
; #define GAS __attribute__((address_space(1)))
; __device__ __forceinline__ unsigned cvt_pk_bf16(float lo, float hi) { unsigned r; asm volatile("v_cvt_pk_bf16_f32 %0, %1, %2" : "=v"(r) : "v"(lo), "v"(hi)); return r; }
; template <bool X8>
; __device__ __forceinline__ void ln_router_phase(Frame& F, int layer) {
;     ...
;                 const float rstd = rsqrtf(wave_sum(s2) * (1.0f / D_MODEL) + LN_EPS);
; #pragma unroll
;                 for (int j = 0; j < 4; ++j) { const int c = 8 * lane + 512 * j;
;                     const f32x4 y0 = ys[tt][j][0] * rstd * *(const GAS f32x4*)(g1 + c) + *(const GAS f32x4*)(b1 + c), y1 = ys[tt][j][1] * rstd * *(const GAS f32x4*)(g1 + c + 4) + *(const GAS f32x4*)(b1 + c + 4);
;                     u32x4 o; o.x = cvt_pk_bf16(y0[0], y0[1]); o.y = cvt_pk_bf16(y0[2], y0[3]); o.z = cvt_pk_bf16(y1[0], y1[1]); o.w = cvt_pk_bf16(y1[2], y1[3]);
;                     *(GAS u32x4*)(X1B + token * D_MODEL + c) = o;
;                     if constexpr (X8) { u32x2 w8; int q8 = __builtin_amdgcn_cvt_pk_fp8_f32(y0[0], y0[1], 0, false); q8 = __builtin_amdgcn_cvt_pk_fp8_f32(y0[2], y0[3], q8, true); w8.x = (unsigned)q8;
;                         q8 = __builtin_amdgcn_cvt_pk_fp8_f32(y1[0], y1[1], 0, false); q8 = __builtin_amdgcn_cvt_pk_fp8_f32(y1[2], y1[3], q8, true); w8.y = (unsigned)q8;
;                         *(GAS u32x2*)(X1B8 + token * D_MODEL + c) = w8; } }
	v_add_f32_e32 v45, v45, v47
	ds_bpermute_b32 v47, v168, v45
	v_fmac_f32_e32 v118, 0xba000000, v43
	v_fmac_f32_e32 v117, 0xba000000, v43
	v_fmac_f32_e32 v119, 0xba000000, v43
	v_fmac_f32_e32 v142, 0xba000000, v43
	s_waitcnt lgkmcnt(0)
	v_add_f32_e32 v45, v45, v47
	ds_bpermute_b32 v47, v169, v45
	v_fmac_f32_e32 v143, 0xba000000, v43
	v_fmac_f32_e32 v115, 0xba000000, v43
	v_fmac_f32_e32 v112, 0xba000000, v43
	v_fmac_f32_e32 v108, 0xba000000, v43
	s_waitcnt lgkmcnt(0)
	v_add_f32_e32 v45, v45, v47
	v_fmamk_f32 v45, v45, 0x3a000000, v184
	v_mul_f32_e32 v47, 0x4b800000, v45
	v_cmp_gt_f32_e32 vcc, s33, v45
	v_fmac_f32_e32 v110, 0xba000000, v43
	v_fmac_f32_e32 v106, 0xba000000, v43
	v_cndmask_b32_e32 v45, v45, v47, vcc
	v_rsq_f32_e32 v45, v45
	v_fmac_f32_e32 v114, 0xba000000, v43
	v_fmac_f32_e32 v26, 0xba000000, v43
	v_fmac_f32_e32 v40, 0xba000000, v43
	v_mul_f32_e32 v47, 0x45800000, v45
	v_cndmask_b32_e32 v202, v45, v47, vcc
	v_pk_mul_f32 v[204:205], v[218:219], v[202:203] op_sel_hi:[1,0]
	v_pk_mul_f32 v[210:211], v[216:217], v[202:203] op_sel_hi:[1,0]
	v_pk_fma_f32 v[10:11], v[10:11], v[204:205], v[14:15]
	v_pk_fma_f32 v[6:7], v[2:3], v[210:211], v[6:7]
	v_cvt_pk_fp8_f32 v32, v10, v11
	v_cvt_pk_fp8_f32 v33, v6, v7
	v_pk_mul_f32 v[208:209], v[222:223], v[202:203] op_sel_hi:[1,0]
	v_pk_mul_f32 v[206:207], v[206:207], v[202:203] op_sel_hi:[1,0]
	v_pk_fma_f32 v[12:13], v[12:13], v[208:209], v[16:17]
	v_pk_fma_f32 v[8:9], v[4:5], v[206:207], v[8:9]
	v_cvt_pk_fp8_f32 v32, v12, v13 op_sel:[0,0,1]
	v_cvt_pk_fp8_f32 v33, v8, v9 op_sel:[0,0,1]
	v_cvt_pk_bf16_f32 v2, v10, v11
	v_cvt_pk_bf16_f32 v3, v12, v13
	v_cvt_pk_bf16_f32 v4, v6, v7
	v_cvt_pk_bf16_f32 v5, v8, v9
	global_store_dwordx4 v[126:127], v[2:5], off
	global_store_dwordx2 v[124:125], v[32:33], off
	ds_read_b128 v[2:5], v240 offset:10240
	s_nop 0
	ds_read_b128 v[6:9], v240 offset:2048
	ds_read_b128 v[10:13], v240 offset:3072
	ds_read_b128 v[14:17], v240 offset:11264
	v_pk_mul_f32 v[32:33], v[214:215], v[202:203] op_sel_hi:[1,0]
	v_pk_mul_f32 v[162:163], v[162:163], v[202:203] op_sel_hi:[1,0]
	v_pk_mul_f32 v[204:205], v[212:213], v[202:203] op_sel_hi:[1,0]
	v_pk_mul_f32 v[164:165], v[164:165], v[202:203] op_sel_hi:[1,0]
	v_pk_mul_f32 v[148:149], v[148:149], v[202:203] op_sel_hi:[1,0]
	v_pk_mul_f32 v[156:157], v[160:161], v[202:203] op_sel_hi:[1,0]
	v_pk_mul_f32 v[150:151], v[150:151], v[202:203] op_sel_hi:[1,0]
	v_pk_mul_f32 v[158:159], v[228:229], v[202:203] op_sel_hi:[1,0]
	v_pk_mul_f32 v[128:129], v[128:129], v[202:203] op_sel_hi:[1,0]
	v_pk_mul_f32 v[132:133], v[132:133], v[202:203] op_sel_hi:[1,0]
	v_pk_mul_f32 v[130:131], v[130:131], v[202:203] op_sel_hi:[1,0]
	v_pk_mul_f32 v[134:135], v[134:135], v[202:203] op_sel_hi:[1,0]
	v_mul_f32_e32 v206, v118, v118
	v_mov_b32_e32 v208, v115
	v_mov_b32_e32 v209, v143
	v_mov_b32_e32 v115, v142
	v_fmac_f32_e32 v27, 0xba000000, v43
	v_fmac_f32_e32 v41, 0xba000000, v43
	v_mul_f32_e32 v142, v26, v26
	v_mul_f32_e32 v210, v40, v40
	v_fmac_f32_e32 v48, 0xba000000, v43
	v_fmac_f32_e32 v44, 0xba000000, v43
	v_fmac_f32_e32 v46, 0xba000000, v43
	v_fmac_f32_e32 v42, 0xba000000, v43
	v_pk_fma_f32 v[142:143], v[26:27], v[26:27], v[142:143] op_sel_hi:[1,1,0]
	v_mov_b32_e32 v107, v110
	v_mul_f32_e32 v142, v42, v42
	v_mov_b32_e32 v109, v112
	v_mov_b32_e32 v43, v46
	v_mov_b32_e32 v45, v48
	s_waitcnt lgkmcnt(0)
	v_pk_fma_f32 v[6:7], v[6:7], v[32:33], v[2:3]
	s_nop 0
	v_cvt_pk_fp8_f32 v36, v6, v7
	v_pk_fma_f32 v[10:11], v[10:11], v[162:163], v[14:15]
	v_pk_fma_f32 v[8:9], v[8:9], v[204:205], v[4:5]
	v_cvt_pk_fp8_f32 v37, v10, v11
	v_pk_fma_f32 v[12:13], v[12:13], v[164:165], v[16:17]
	v_cvt_pk_fp8_f32 v36, v8, v9 op_sel:[0,0,1]
	v_cvt_pk_bf16_f32 v2, v6, v7
	v_cvt_pk_fp8_f32 v37, v12, v13 op_sel:[0,0,1]
	v_cvt_pk_bf16_f32 v3, v8, v9
	v_cvt_pk_bf16_f32 v4, v10, v11
	v_cvt_pk_bf16_f32 v5, v12, v13
	global_store_dwordx4 v[126:127], v[2:5], off offset:1024
	global_store_dwordx2 v[124:125], v[36:37], off offset:512
	ds_read_b128 v[2:5], v240 offset:12288
	s_nop 0
	ds_read_b128 v[6:9], v240 offset:4096
	ds_read_b128 v[10:13], v240 offset:5120
	ds_read_b128 v[14:17], v240 offset:13312
	v_mov_b32_e32 v32, v154
	v_mov_b32_e32 v33, v152
	v_mov_b32_e32 v36, v155
	v_mov_b32_e32 v37, v153
	v_mov_b32_e32 v162, v155
	v_mov_b32_e32 v163, v154
	v_mov_b32_e32 v154, v153
	v_mov_b32_e32 v155, v152
	v_mov_b32_e32 v152, v144
	v_mov_b32_e32 v153, v140
	v_mov_b32_e32 v164, v145
	v_mov_b32_e32 v165, v141
	v_mov_b32_e32 v204, v145
	v_mov_b32_e32 v205, v144
	v_mov_b32_e32 v144, v141
	v_mov_b32_e32 v145, v140
	v_mov_b32_e32 v140, v123
	v_mov_b32_e32 v141, v147
	v_mov_b32_e32 v123, v146
	v_pk_mul_f32 v[136:137], v[144:145], v[144:145]
	v_pk_mul_f32 v[138:139], v[140:141], v[140:141]
	v_pk_mul_f32 v[144:145], v[122:123], v[122:123]
	v_pk_fma_f32 v[136:137], v[204:205], v[204:205], v[136:137]
	v_mul_f32_e32 v146, v116, v116
	v_pk_fma_f32 v[146:147], v[116:117], v[116:117], v[146:147] op_sel_hi:[1,1,0]
	s_waitcnt lgkmcnt(0)
; #define GAS __attribute__((address_space(1)))
; __device__ __forceinline__ unsigned cvt_pk_bf16(float lo, float hi) { unsigned r; asm volatile("v_cvt_pk_bf16_f32 %0, %1, %2" : "=v"(r) : "v"(lo), "v"(hi)); return r; }
; template <bool X8>
; __device__ __forceinline__ void ln_router_phase(Frame& F, int layer) {
;     ...
;                 const float mean = wave_sum(s) * (1.0f / D_MODEL); float s2 = 0.f;
; #pragma unroll
;                 for (int j = 0; j < 4; ++j)
; #pragma unroll
;                     for (int h = 0; h < 2; ++h) { ys[tt][j][h] = ys[tt][j][h] - mean; s2 += (ys[tt][j][h][0] * ys[tt][j][h][0] + ys[tt][j][h][1] * ys[tt][j][h][1]) + (ys[tt][j][h][2] * ys[tt][j][h][2] + ys[tt][j][h][3] * ys[tt][j][h][3]); }
;                 const float rstd = rsqrtf(wave_sum(s2) * (1.0f / D_MODEL) + LN_EPS);
; #pragma unroll
;                 for (int j = 0; j < 4; ++j) { const int c = 8 * lane + 512 * j;
;                     const f32x4 y0 = ys[tt][j][0] * rstd * *(const GAS f32x4*)(g1 + c) + *(const GAS f32x4*)(b1 + c), y1 = ys[tt][j][1] * rstd * *(const GAS f32x4*)(g1 + c + 4) + *(const GAS f32x4*)(b1 + c + 4);
;                     u32x4 o; o.x = cvt_pk_bf16(y0[0], y0[1]); o.y = cvt_pk_bf16(y0[2], y0[3]); o.z = cvt_pk_bf16(y1[0], y1[1]); o.w = cvt_pk_bf16(y1[2], y1[3]);
;                     *(GAS u32x4*)(X1B + token * D_MODEL + c) = o;
;                     if constexpr (X8) { u32x2 w8; int q8 = __builtin_amdgcn_cvt_pk_fp8_f32(y0[0], y0[1], 0, false); q8 = __builtin_amdgcn_cvt_pk_fp8_f32(y0[2], y0[3], q8, true); w8.x = (unsigned)q8;
;                         q8 = __builtin_amdgcn_cvt_pk_fp8_f32(y1[0], y1[1], 0, false); q8 = __builtin_amdgcn_cvt_pk_fp8_f32(y1[2], y1[3], q8, true); w8.y = (unsigned)q8;
;                         *(GAS u32x2*)(X1B8 + token * D_MODEL + c) = w8; } }
	v_pk_fma_f32 v[6:7], v[6:7], v[148:149], v[2:3]
	s_nop 0
	v_cvt_pk_fp8_f32 v34, v6, v7
	v_pk_fma_f32 v[10:11], v[156:157], v[10:11], v[14:15]
	v_pk_fma_f32 v[8:9], v[8:9], v[150:151], v[4:5]
	v_cvt_pk_fp8_f32 v35, v10, v11
	v_pk_fma_f32 v[12:13], v[158:159], v[12:13], v[16:17]
	v_cvt_pk_fp8_f32 v34, v8, v9 op_sel:[0,0,1]
	v_cvt_pk_bf16_f32 v2, v6, v7
	v_cvt_pk_fp8_f32 v35, v12, v13 op_sel:[0,0,1]
	v_cvt_pk_bf16_f32 v3, v8, v9
	v_cvt_pk_bf16_f32 v4, v10, v11
	v_cvt_pk_bf16_f32 v5, v12, v13
	global_store_dwordx4 v[126:127], v[2:5], off offset:2048
	global_store_dwordx2 v[124:125], v[34:35], off offset:1024
	ds_read_b128 v[2:5], v240 offset:14336
	s_nop 0
	ds_read_b128 v[6:9], v240 offset:6144
	ds_read_b128 v[10:13], v240 offset:7168
	ds_read_b128 v[14:17], v240 offset:15360
	v_pk_mul_f32 v[34:35], v[154:155], v[154:155]
	v_pk_mov_b32 v[158:159], v[144:145], v[138:139] op_sel:[1,0]
	v_pk_fma_f32 v[34:35], v[162:163], v[162:163], v[34:35]
	v_mov_b32_e32 v145, v139
	v_pk_add_f32 v[34:35], v[34:35], v[136:137]
	v_pk_add_f32 v[136:137], v[158:159], v[144:145]
	v_pk_fma_f32 v[148:149], v[118:119], v[118:119], v[206:207] op_sel_hi:[1,1,0]
	v_pk_add_f32 v[34:35], v[34:35], v[34:35] op_sel_hi:[0,1]
	v_pk_add_f32 v[136:137], v[136:137], v[136:137] op_sel_hi:[0,1]
	v_pk_mul_f32 v[150:151], v[208:209], v[208:209]
	v_pk_mul_f32 v[154:155], v[114:115], v[114:115]
	v_mul_f32_e32 v146, v106, v106
	v_mul_f32_e32 v148, v110, v110
	v_mul_f32_e32 v136, v108, v108
	v_mul_f32_e32 v34, v112, v112
	v_pk_mov_b32 v[138:139], v[154:155], v[150:151] op_sel:[1,0]
	v_mov_b32_e32 v155, v151
	v_pk_add_f32 v[144:145], v[146:147], v[148:149]
	v_pk_add_f32 v[34:35], v[136:137], v[34:35]
	v_pk_add_f32 v[138:139], v[138:139], v[154:155]
	v_pk_add_f32 v[34:35], v[144:145], v[34:35]
	v_pk_fma_f32 v[156:157], v[40:41], v[40:41], v[210:211] op_sel_hi:[1,1,0]
	v_pk_add_f32 v[138:139], v[138:139], v[138:139] op_sel_hi:[0,1]
	v_pk_add_f32 v[34:35], v[34:35], v[34:35] op_sel_hi:[0,1]
	v_mul_f32_e32 v156, v46, v46
	v_mul_f32_e32 v138, v44, v44
	v_mul_f32_e32 v34, v48, v48
	v_pk_add_f32 v[142:143], v[142:143], v[156:157]
	v_pk_add_f32 v[34:35], v[138:139], v[34:35]
	s_waitcnt lgkmcnt(0)
	v_pk_fma_f32 v[6:7], v[128:129], v[6:7], v[2:3]
	s_nop 0
	v_cvt_pk_fp8_f32 v30, v6, v7
	v_pk_fma_f32 v[10:11], v[132:133], v[10:11], v[14:15]
	v_pk_fma_f32 v[8:9], v[130:131], v[8:9], v[4:5]
	v_cvt_pk_fp8_f32 v31, v10, v11
	v_pk_fma_f32 v[12:13], v[134:135], v[12:13], v[16:17]
	v_cvt_pk_fp8_f32 v30, v8, v9 op_sel:[0,0,1]
	v_cvt_pk_bf16_f32 v2, v6, v7
	v_cvt_pk_fp8_f32 v31, v12, v13 op_sel:[0,0,1]
	v_cvt_pk_bf16_f32 v3, v8, v9
	v_cvt_pk_bf16_f32 v4, v10, v11
	v_cvt_pk_bf16_f32 v5, v12, v13
	global_store_dwordx4 v[126:127], v[2:5], off offset:3072
	global_store_dwordx2 v[124:125], v[30:31], off offset:1536
	ds_read_b128 v[2:5], v240 offset:8192
	s_nop 0
	ds_read_b128 v[6:9], v240 offset:0
	ds_read_b128 v[10:13], v240 offset:1024
	ds_read_b128 v[14:17], v240 offset:9216
	v_pk_add_f32 v[34:35], v[142:143], v[34:35]
	s_nop 0
	v_add_f32_e32 v30, v34, v35
	ds_bpermute_b32 v31, v53, v30
	s_waitcnt lgkmcnt(0)
	v_add_f32_e32 v30, v30, v31
	ds_bpermute_b32 v31, v89, v30
	s_waitcnt lgkmcnt(0)
	v_add_f32_e32 v30, v30, v31
	ds_bpermute_b32 v31, v166, v30
	s_waitcnt lgkmcnt(0)
	v_add_f32_e32 v30, v30, v31
	ds_bpermute_b32 v31, v167, v30
	s_waitcnt lgkmcnt(0)
	v_add_f32_e32 v30, v30, v31
	ds_bpermute_b32 v31, v168, v30
	s_waitcnt lgkmcnt(0)
	v_add_f32_e32 v30, v30, v31
	ds_bpermute_b32 v31, v169, v30
	s_waitcnt lgkmcnt(0)
	v_add_f32_e32 v30, v30, v31
	v_fmamk_f32 v30, v30, 0x3a000000, v184
	v_mul_f32_e32 v31, 0x4b800000, v30
	v_cmp_gt_f32_e32 vcc, s33, v30
	s_nop 1
	v_cndmask_b32_e32 v30, v30, v31, vcc
	v_rsq_f32_e32 v30, v30
	s_nop 0
	v_mul_f32_e32 v31, 0x45800000, v30
	v_cndmask_b32_e32 v30, v30, v31, vcc
	v_pk_mul_f32 v[34:35], v[36:37], v[30:31] op_sel_hi:[1,0]
	v_pk_mul_f32 v[32:33], v[32:33], v[30:31] op_sel_hi:[1,0]
	v_pk_mul_f32 v[36:37], v[164:165], v[30:31] op_sel_hi:[1,0]
	v_pk_mul_f32 v[124:125], v[152:153], v[30:31] op_sel_hi:[1,0]
	v_pk_mul_f32 v[116:117], v[116:117], v[30:31] op_sel_hi:[1,0]
	v_pk_mul_f32 v[118:119], v[118:119], v[30:31] op_sel_hi:[1,0]
	v_pk_mul_f32 v[26:27], v[26:27], v[30:31] op_sel_hi:[1,0]
	s_waitcnt lgkmcnt(0)
	v_pk_fma_f32 v[6:7], v[6:7], v[34:35], v[2:3]
	s_nop 0
	v_cvt_pk_fp8_f32 v120, v6, v7
	v_pk_fma_f32 v[10:11], v[10:11], v[32:33], v[14:15]
	v_pk_fma_f32 v[8:9], v[8:9], v[36:37], v[4:5]
	v_cvt_pk_fp8_f32 v121, v10, v11
	v_pk_fma_f32 v[12:13], v[12:13], v[124:125], v[16:17]
	v_cvt_pk_fp8_f32 v120, v8, v9 op_sel:[0,0,1]
	v_cvt_pk_bf16_f32 v2, v6, v7
	v_cvt_pk_fp8_f32 v121, v12, v13 op_sel:[0,0,1]
	v_cvt_pk_bf16_f32 v3, v8, v9
	v_cvt_pk_bf16_f32 v4, v10, v11
	v_cvt_pk_bf16_f32 v5, v12, v13
	global_store_dwordx4 v[28:29], v[2:5], off
	global_store_dwordx2 v[38:39], v[120:121], off
	ds_read_b128 v[2:5], v240 offset:10240
	s_nop 0
	ds_read_b128 v[6:9], v240 offset:2048
	ds_read_b128 v[10:13], v240 offset:3072
	ds_read_b128 v[14:17], v240 offset:11264
	v_pk_mul_f32 v[34:35], v[122:123], v[30:31] op_sel_hi:[1,0]
	v_mov_b32_e32 v32, 0
	v_mov_b32_e32 v33, 0
	v_pk_mul_f32 v[36:37], v[140:141], v[30:31] op_sel_hi:[1,0]
	s_waitcnt lgkmcnt(0)
; #define GAS __attribute__((address_space(1)))
; #define VM_WAIT() asm volatile("s_waitcnt vmcnt(0)" ::: "memory")
; __device__ __forceinline__ unsigned cvt_pk_bf16(float lo, float hi) { unsigned r; asm volatile("v_cvt_pk_bf16_f32 %0, %1, %2" : "=v"(r) : "v"(lo), "v"(hi)); return r; }
; template <bool X8>
; __device__ __forceinline__ void ln_router_phase(Frame& F, int layer) {
;     ...
; #pragma unroll
;                 for (int j = 0; j < 4; ++j) { const int c = 8 * lane + 512 * j;
;                     const f32x4 y0 = ys[tt][j][0] * rstd * *(const GAS f32x4*)(g1 + c) + *(const GAS f32x4*)(b1 + c), y1 = ys[tt][j][1] * rstd * *(const GAS f32x4*)(g1 + c + 4) + *(const GAS f32x4*)(b1 + c + 4);
;                     u32x4 o; o.x = cvt_pk_bf16(y0[0], y0[1]); o.y = cvt_pk_bf16(y0[2], y0[3]); o.z = cvt_pk_bf16(y1[0], y1[1]); o.w = cvt_pk_bf16(y1[2], y1[3]);
;                     *(GAS u32x4*)(X1B + token * D_MODEL + c) = o;
;                     if constexpr (X8) { u32x2 w8; int q8 = __builtin_amdgcn_cvt_pk_fp8_f32(y0[0], y0[1], 0, false); q8 = __builtin_amdgcn_cvt_pk_fp8_f32(y0[2], y0[3], q8, true); w8.x = (unsigned)q8;
;                         q8 = __builtin_amdgcn_cvt_pk_fp8_f32(y1[0], y1[1], 0, false); q8 = __builtin_amdgcn_cvt_pk_fp8_f32(y1[2], y1[3], q8, true); w8.y = (unsigned)q8;
;                         *(GAS u32x2*)(X1B8 + token * D_MODEL + c) = w8; } }
;             }
;         }
;         VM_WAIT(); __syncthreads();
;         f32x4 dacc[4];
; #pragma unroll
;         for (int nb = 0; nb < 4; ++nb) dacc[nb] = (f32x4){0.f, 0.f, 0.f, 0.f};
;         const int tt4 = w & 3, kh = w >> 2;
;         u32x4 xr[4], wq[4];
;         const GAS bf16_t* wrb = (const GAS bf16_t*)(F.ws + WS_WRB) + (size_t)layer * D_MODEL * N_EXPERTS;
; #pragma unroll
;         for (int j = 0; j < 4; ++j) { const int idx = tid + 512 * j, row = idx >> 5, c8 = idx & 31; xr[j] = *(const GAS u32x4*)(X1B + (size_t)(tok0 + row) * D_MODEL + 8 * c8); }
; #pragma unroll
;         for (int j = 0; j < 4; ++j) { const int idx = tid + 512 * j, row = idx >> 3, c8 = idx & 7; wq[j] = *(const GAS u32x4*)(wrb + (size_t)row * N_EXPERTS + 8 * c8); }
	v_pk_fma_f32 v[6:7], v[6:7], v[34:35], v[2:3]
	s_nop 0
	v_cvt_pk_fp8_f32 v32, v6, v7
	v_pk_fma_f32 v[10:11], v[10:11], v[116:117], v[14:15]
	v_pk_fma_f32 v[8:9], v[8:9], v[36:37], v[4:5]
	v_cvt_pk_fp8_f32 v33, v10, v11
	v_pk_fma_f32 v[12:13], v[12:13], v[118:119], v[16:17]
	v_cvt_pk_fp8_f32 v32, v8, v9 op_sel:[0,0,1]
	v_cvt_pk_bf16_f32 v2, v6, v7
	v_cvt_pk_fp8_f32 v33, v12, v13 op_sel:[0,0,1]
	v_cvt_pk_bf16_f32 v3, v8, v9
	v_cvt_pk_bf16_f32 v4, v10, v11
	v_cvt_pk_bf16_f32 v5, v12, v13
	global_store_dwordx4 v[28:29], v[2:5], off offset:1024
	global_store_dwordx2 v[38:39], v[32:33], off offset:512
	ds_read_b128 v[2:5], v240 offset:12288
	s_nop 0
	ds_read_b128 v[6:9], v240 offset:4096
	ds_read_b128 v[10:13], v240 offset:5120
	ds_read_b128 v[14:17], v240 offset:13312
	v_pk_mul_f32 v[34:35], v[106:107], v[30:31] op_sel_hi:[1,0]
	v_pk_mul_f32 v[106:107], v[114:115], v[30:31] op_sel_hi:[1,0]
	v_mov_b32_e32 v32, 0
	v_mov_b32_e32 v33, 0
	v_pk_mul_f32 v[36:37], v[108:109], v[30:31] op_sel_hi:[1,0]
	v_pk_mul_f32 v[108:109], v[208:209], v[30:31] op_sel_hi:[1,0]
	s_waitcnt lgkmcnt(0)
	v_pk_fma_f32 v[6:7], v[34:35], v[6:7], v[2:3]
	s_nop 0
	v_cvt_pk_fp8_f32 v32, v6, v7
	v_pk_fma_f32 v[10:11], v[106:107], v[10:11], v[14:15]
	v_pk_fma_f32 v[8:9], v[36:37], v[8:9], v[4:5]
	v_cvt_pk_fp8_f32 v33, v10, v11
	v_pk_fma_f32 v[12:13], v[108:109], v[12:13], v[16:17]
	v_cvt_pk_fp8_f32 v32, v8, v9 op_sel:[0,0,1]
	v_cvt_pk_bf16_f32 v2, v6, v7
	v_cvt_pk_fp8_f32 v33, v12, v13 op_sel:[0,0,1]
	v_cvt_pk_bf16_f32 v3, v8, v9
	v_cvt_pk_bf16_f32 v4, v10, v11
	v_cvt_pk_bf16_f32 v5, v12, v13
	global_store_dwordx4 v[28:29], v[2:5], off offset:2048
	global_store_dwordx2 v[38:39], v[32:33], off offset:1024
	ds_read_b128 v[2:5], v240 offset:14336
	s_nop 0
	ds_read_b128 v[6:9], v240 offset:6144
	ds_read_b128 v[10:13], v240 offset:7168
	ds_read_b128 v[14:17], v240 offset:15360
	v_pk_mul_f32 v[34:35], v[40:41], v[30:31] op_sel_hi:[1,0]
	v_pk_mul_f32 v[36:37], v[42:43], v[30:31] op_sel_hi:[1,0]
	v_mov_b32_e32 v32, 0
	v_mov_b32_e32 v33, 0
	v_pk_mul_f32 v[30:31], v[44:45], v[30:31] op_sel_hi:[1,0]
	s_waitcnt lgkmcnt(0)
	v_pk_fma_f32 v[4:5], v[34:35], v[8:9], v[4:5]
	v_pk_fma_f32 v[2:3], v[26:27], v[6:7], v[2:3]
	v_pk_fma_f32 v[8:9], v[36:37], v[10:11], v[14:15]
	v_cvt_pk_fp8_f32 v32, v2, v3
	v_cvt_pk_fp8_f32 v33, v8, v9
	v_pk_fma_f32 v[6:7], v[30:31], v[12:13], v[16:17]
	v_cvt_pk_bf16_f32 v2, v2, v3
	v_cvt_pk_fp8_f32 v32, v4, v5 op_sel:[0,0,1]
	v_cvt_pk_fp8_f32 v33, v6, v7 op_sel:[0,0,1]
	v_cvt_pk_bf16_f32 v3, v4, v5
	v_cvt_pk_bf16_f32 v4, v8, v9
	v_cvt_pk_bf16_f32 v5, v6, v7
	global_store_dwordx4 v[28:29], v[2:5], off offset:3072
	global_store_dwordx2 v[38:39], v[32:33], off offset:1536
	s_cbranch_scc0 .LBB0_1308
	s_lshl_b32 s82, s0, 6
	v_add_u32_e32 v2, s82, v173
	v_add_u32_e32 v4, s82, v174
	v_add_u32_e32 v10, s82, v175
	v_add_u32_e32 v12, s82, v176
	v_ashrrev_i32_e32 v3, 31, v2
	v_ashrrev_i32_e32 v5, 31, v4
	v_ashrrev_i32_e32 v11, 31, v10
	v_ashrrev_i32_e32 v13, 31, v12
	v_lshlrev_b64 v[2:3], 12, v[2:3]
	v_lshlrev_b64 v[4:5], 12, v[4:5]
	v_lshlrev_b64 v[10:11], 12, v[10:11]
	v_lshlrev_b64 v[12:13], 12, v[12:13]
	v_lshl_add_u64 v[2:3], v[56:57], 0, v[2:3]
	v_lshl_add_u64 v[6:7], v[56:57], 0, v[4:5]
	v_lshl_add_u64 v[10:11], v[56:57], 0, v[10:11]
	v_lshl_add_u64 v[14:15], v[56:57], 0, v[12:13]
	s_waitcnt vmcnt(0)
	s_barrier
	global_load_dwordx4 v[2:5], v[2:3], off
	s_nop 0
	global_load_dwordx4 v[6:9], v[6:7], off
	s_nop 0
	global_load_dwordx4 v[10:13], v[10:11], off
	s_nop 0
	global_load_dwordx4 v[14:17], v[14:15], off
	s_nop 0
	global_load_dwordx4 v[18:21], v[80:81], off
	global_load_dwordx4 v[22:25], v[82:83], off
	global_load_dwordx4 v[26:29], v[84:85], off
	global_load_dwordx4 v[30:33], v[86:87], off
	v_ashrrev_i32_e32 v99, 31, v98
	v_lshlrev_b64 v[34:35], 12, v[98:99]
	v_ashrrev_i32_e32 v101, 31, v100
	v_lshl_add_u64 v[106:107], v[54:55], 0, v[34:35]
	v_lshlrev_b64 v[34:35], 12, v[100:101]
	v_ashrrev_i32_e32 v103, 31, v102
	v_lshl_add_u64 v[108:109], v[54:55], 0, v[34:35]
	v_lshlrev_b64 v[34:35], 12, v[102:103]
	v_ashrrev_i32_e32 v105, 31, v104
	v_lshl_add_u64 v[110:111], v[54:55], 0, v[34:35]
	v_lshlrev_b64 v[34:35], 12, v[104:105]
	v_lshl_add_u64 v[112:113], v[54:55], 0, v[34:35]
	v_mov_b32_e32 v34, 0
	s_mov_b32 s20, 8
	v_mov_b64_e32 v[114:115], v[96:97]
	v_mov_b64_e32 v[116:117], v[94:95]
	v_mov_b64_e32 v[118:119], v[92:93]
	v_mov_b64_e32 v[120:121], v[90:91]
	v_mov_b32_e32 v35, v34
	v_mov_b32_e32 v36, v34
	v_mov_b32_e32 v37, v34
	v_mov_b32_e32 v42, v34
	v_mov_b32_e32 v43, v34
	v_mov_b32_e32 v44, v34
	v_mov_b32_e32 v45, v34
	v_mov_b32_e32 v46, v34
	v_mov_b32_e32 v47, v34
	v_mov_b32_e32 v48, v34
	v_mov_b32_e32 v49, v34
	v_mov_b32_e32 v38, v34
	v_mov_b32_e32 v39, v34
	v_mov_b32_e32 v40, v34
	v_mov_b32_e32 v41, v34
	s_branch .LBB0_1311

; #define GAS __attribute__((address_space(1)))
; template <bool X8>
; __device__ __forceinline__ void ln_router_phase(Frame& F, int layer) {
;     PHASE_ARGS();
;     const GAS bf16_t* R = (const GAS bf16_t*)(F.ws + WS_R); GAS bf16_t* X1B = (GAS bf16_t*)(F.ws + WS_X1B); GAS unsigned char* X1B8 = F.ws + WS_X1B8;
;     const GAS float* g1 = GIN(8) + (size_t)layer * D_MODEL; const GAS float* b1 = GIN(9) + (size_t)layer * D_MODEL;
;     const GAS float* wrt = GIN(10) + (size_t)layer * D_MODEL * N_EXPERTS; const GAS float* rbias = GIN(11) + (size_t)layer * N_EXPERTS;
;     GAS int* PE = (GAS int*)(F.ws + WS_PE); GAS int* PP = (GAS int*)(F.ws + WS_PP); GAS float* PG = (GAS float*)(F.ws + WS_PG); GAS int* RM = (GAS int*)(F.ws + WS_RM);
;     GAS unsigned* cnt = F.ctl + CW_CNT + layer * 64;
;     constexpr int XROW = 528, WROW = 144;
;     LAS unsigned char* XSb = F.lds; LAS unsigned char* WSb = F.lds + 64 * XROW; LAS float* PART = (LAS float*)F.lds; LAS float* LG = (LAS float*)(F.lds + 32768);
;     LAS int* LCNT = (LAS int*)(F.lds + 49152); LAS int* BASE = (LAS int*)(F.lds + 49408); LAS int* PEL = (LAS int*)(F.lds + 49664); LAS int* PLL = (LAS int*)(F.lds + 51712);
;     PHASE_IDS();
;     const int g = lane >> 4, i = lane & 15;
;     for (int bt = F.bid; bt < T / 64; bt += F.G) {
;         const int tok0 = bt * 64;
; #pragma unroll 1
;         for (int pr = 0; pr < 4; ++pr) {
;             f32x4 ys[2][4][2];
; #pragma unroll
;             for (int tt = 0; tt < 2; ++tt) { const size_t token = (size_t)(tok0 + 8 * w + 2 * pr + tt);
;                 const GAS u32x4* rp = (const GAS u32x4*)(R + token * D_MODEL) + lane;
; #pragma unroll
;                 for (int j = 0; j < 4; ++j) { const u32x4 r = rp[64 * j]; ys[tt][j][0] = (f32x4){bflo(r.x), bfhi(r.x), bflo(r.y), bfhi(r.y)}; ys[tt][j][1] = (f32x4){bflo(r.z), bfhi(r.z), bflo(r.w), bfhi(r.w)}; } }
; #pragma unroll
;             for (int tt = 0; tt < 2; ++tt) { const size_t token = (size_t)(tok0 + 8 * w + 2 * pr + tt); float s = 0.f;
; #pragma unroll
;                 for (int j = 0; j < 4; ++j)
; #pragma unroll
;                     for (int h = 0; h < 2; ++h) s += (ys[tt][j][h][0] + ys[tt][j][h][1]) + (ys[tt][j][h][2] + ys[tt][j][h][3]);
;                 const float mean = wave_sum(s) * (1.0f / D_MODEL); float s2 = 0.f;
; #pragma unroll
;                 for (int j = 0; j < 4; ++j)
; #pragma unroll
.LBB0_2868:
	s_cmp_lt_i32 s54, 19
	s_cselect_b64 s[58:59], -1, 0
	s_and_b64 s[0:1], s[58:59], s[4:5]
	s_andn2_b64 vcc, exec, s[0:1]
	s_cbranch_vccnz .LBB0_2892
	v_readlane_b32 s4, v254, 1
	s_mov_b64 s[62:63], s[52:53]
	s_mov_b32 s0, s95
	s_mov_b32 s1, 0
	s_mov_b64 s[6:7], s[52:53]
	v_readlane_b32 s2, v254, 0
	v_readlane_b32 s5, v254, 2
	s_waitcnt vmcnt(0)
	v_mov_b32_e32 v50, v0
	s_mov_b32 s61, 0
	s_cmpk_gt_i32 s2, 0xff
	v_readfirstlane_b32 s12, v50
	s_cbranch_scc1 .LBB0_2892
	v_mbcnt_lo_u32_b32 v2, -1, 0
	v_mbcnt_hi_u32_b32 v2, -1, v2
	v_and_b32_e32 v3, 64, v2
	v_add_u32_e32 v3, 64, v3
	v_xor_b32_e32 v6, 1, v2
	v_cmp_lt_i32_e32 vcc, v6, v3
	s_add_u32 s64, s62, 0x35300000
	s_addc_u32 s65, s63, 0
	v_cndmask_b32_e32 v6, v2, v6, vcc
	v_lshlrev_b32_e32 v53, 2, v6
	v_xor_b32_e32 v6, 2, v2
	v_cmp_lt_i32_e32 vcc, v6, v3
	s_load_dwordx4 s[16:19], s[4:5], 0x40
	s_load_dwordx2 s[14:15], s[4:5], 0x58
	v_cndmask_b32_e32 v6, v2, v6, vcc
	v_lshlrev_b32_e32 v93, 2, v6
	v_xor_b32_e32 v6, 4, v2
	v_cmp_lt_i32_e32 vcc, v6, v3
	s_add_u32 s66, s62, 0x35500000
	s_addc_u32 s67, s63, 0
	v_cndmask_b32_e32 v6, v2, v6, vcc
	v_lshlrev_b32_e32 v170, 2, v6
	v_xor_b32_e32 v6, 8, v2
	v_cmp_lt_i32_e32 vcc, v6, v3
	s_add_u32 s68, s62, 0x35600000
	s_addc_u32 s69, s63, 0
	v_cndmask_b32_e32 v6, v2, v6, vcc
	v_lshlrev_b32_e32 v171, 2, v6
	v_xor_b32_e32 v6, 16, v2
	v_cmp_lt_i32_e32 vcc, v6, v3
	s_waitcnt lgkmcnt(0)
	s_add_u32 s8, s18, 0x2000
	s_addc_u32 s9, s19, 0
	v_cndmask_b32_e32 v6, v2, v6, vcc
	v_lshlrev_b32_e32 v172, 2, v6
	v_xor_b32_e32 v6, 32, v2
	v_cmp_lt_i32_e32 vcc, v6, v3
	v_lshlrev_b32_e32 v7, 4, v50
	s_add_u32 s10, s16, 0x2000
	v_cndmask_b32_e32 v2, v2, v6, vcc
	v_and_b32_e32 v54, 0x1f0, v7
	v_mov_b32_e32 v55, 0
	s_addc_u32 s11, s17, 0
	s_ashr_i32 s13, s12, 6
	v_lshlrev_b32_e32 v173, 2, v2
	v_lshl_add_u64 v[2:3], s[62:63], 0, v[54:55]
	s_mov_b64 s[4:5], 0x31300000
	v_lshl_add_u64 v[56:57], v[2:3], 0, s[4:5]
	s_lshl_b32 s4, s13, 4
	v_and_b32_e32 v4, 15, v50
	s_and_b32 s4, s4, 48
	v_bfe_u32 v5, v50, 4, 2
	v_and_b32_e32 v2, 0x70, v7
	v_or_b32_e32 v7, s4, v4
	s_movk_i32 s17, 0x210
	v_mov_b32_e32 v8, s1
	v_and_b32_e32 v1, 63, v50
	s_ashr_i32 s12, s12, 8
	v_mad_u32_u24 v20, v7, s17, v8
	v_lshlrev_b32_e32 v7, 3, v5
	v_lshlrev_b32_e32 v5, 2, v5
	v_add_u32_e32 v18, s1, v54
	v_lshl_or_b32 v5, s12, 6, v5
	v_ashrrev_i32_e32 v51, 31, v50
	v_lshlrev_b32_e32 v54, 2, v1
	v_and_b32_e32 v27, 7, v50
	v_lshlrev_b32_e32 v6, 3, v50
	v_or_b32_e32 v24, s4, v5
	v_lshl_add_u32 v25, v4, 2, s1
	v_add_u32_e32 v176, s1, v54
	v_lshl_add_u64 v[58:59], s[14:15], 0, v[54:55]
	v_lshl_add_u64 v[4:5], v[50:51], 2, s[6:7]
	s_mov_b64 s[6:7], 0x1100
	v_lshlrev_b32_e32 v54, 2, v27
	s_add_i32 s16, s1, 0x8400
	v_bfe_u32 v3, v50, 2, 2
	v_lshl_or_b32 v21, s12, 7, v7
	v_and_b32_e32 v6, 24, v6
	v_lshl_add_u64 v[62:63], v[4:5], 0, s[6:7]
	v_lshl_add_u64 v[4:5], s[62:63], 0, v[54:55]
	s_mov_b64 s[6:7], 0x35400000
	v_lshlrev_b32_e32 v54, 5, v1
	v_add_u32_e32 v22, s16, v6
	v_ashrrev_i32_e32 v64, 3, v50
	v_lshl_add_u64 v[66:67], v[4:5], 0, s[6:7]
	v_or_b32_e32 v4, 0x800, v54
	v_mov_b32_e32 v5, v55
	s_movk_i32 s6, 0x90
	v_or_b32_e32 v31, v21, v3
	v_add_u32_e32 v23, 0x240, v22
	v_lshl_add_u64 v[72:73], s[10:11], 0, v[4:5]
	v_lshl_add_u64 v[74:75], s[8:9], 0, v[4:5]
	v_or_b32_e32 v4, 0x1000, v54
	v_ashrrev_i32_e32 v65, 31, v64
	v_mul_lo_u32 v31, v31, s6
	v_lshl_add_u64 v[76:77], s[10:11], 0, v[4:5]
	v_lshl_add_u64 v[78:79], s[8:9], 0, v[4:5]
	v_lshlrev_b64 v[4:5], 7, v[64:65]
	v_add_u32_e32 v65, v31, v22
	v_add_u32_e32 v181, v31, v23
	v_or_b32_e32 v31, 32, v21
	v_lshlrev_b32_e32 v32, 1, v31
	v_or_b32_e32 v31, v31, v3
	v_mul_lo_u32 v31, v31, s6
	v_lshlrev_b32_e32 v30, 1, v21
	v_add_u32_e32 v182, v31, v22
	v_add_u32_e32 v183, v31, v23
	v_or_b32_e32 v31, 64, v21
	v_or_b32_e32 v21, 0x60, v21
	v_lshlrev_b32_e32 v33, 1, v31
	v_or_b32_e32 v31, v31, v3
	v_or_b32_e32 v3, v21, v3
	v_add_u32_e32 v6, 0x200, v50
	v_add_u32_e32 v10, 0x400, v50
	v_add_u32_e32 v14, 0x600, v50
	v_mul_lo_u32 v3, v3, s6
	v_ashrrev_i32_e32 v178, 5, v6
	v_ashrrev_i32_e32 v179, 5, v10
	v_ashrrev_i32_e32 v180, 5, v14
	v_ashrrev_i32_e32 v6, 3, v6
	v_ashrrev_i32_e32 v10, 3, v10
	v_ashrrev_i32_e32 v14, 3, v14
	v_add_u32_e32 v186, v3, v22
	v_add_u32_e32 v187, v3, v23
	v_mov_b32_e32 v3, v55
	v_add_u32_e32 v19, s1, v2
	v_ashrrev_i32_e32 v7, 31, v6
	v_ashrrev_i32_e32 v11, 31, v10
	v_ashrrev_i32_e32 v15, 31, v14
	v_lshl_add_u64 v[2:3], s[62:63], 0, v[2:3]
	s_mov_b64 s[20:21], 0x1d250000
	v_lshlrev_b64 v[8:9], 7, v[6:7]
	v_lshlrev_b64 v[12:13], 7, v[10:11]
	v_lshlrev_b64 v[16:17], 7, v[14:15]
	v_lshl_add_u64 v[2:3], v[2:3], 0, s[20:21]
	s_lshl_b32 s3, s13, 3
	v_ashrrev_i32_e32 v177, 5, v50
	v_mul_lo_u32 v31, v31, s6
	v_lshl_add_u64 v[84:85], v[2:3], 0, v[4:5]
	v_lshl_add_u64 v[86:87], v[2:3], 0, v[8:9]
	v_lshl_add_u64 v[88:89], v[2:3], 0, v[12:13]
	v_lshl_add_u64 v[90:91], v[2:3], 0, v[16:17]
	s_lshl_b32 s22, s2, 6
	v_lshlrev_b32_e32 v2, 4, v27
	v_and_b32_e32 v26, 56, v50
	s_mov_b64 s[12:13], 0xff
	v_lshl_add_u64 v[68:69], s[10:11], 0, v[54:55]
	v_lshl_add_u64 v[70:71], s[8:9], 0, v[54:55]
	v_lshlrev_b32_e32 v252, 4, v50
	v_mov_b32_e32 v253, 0
	v_lshl_add_u64 v[244:245], s[10:11], 0, v[252:253]
	v_lshl_add_u64 v[252:253], s[8:9], 0, v[252:253]
	global_load_dwordx4 v[244:247], v[244:245], off
	global_load_dwordx4 v[248:251], v[252:253], off
	v_lshrrev_b32_e32 v255, 7, v50
	v_lshlrev_b32_e32 v255, 11, v255
	v_and_b32_e32 v205, 1, v50
	v_lshl_or_b32 v255, v205, 10, v255
	v_bfe_u32 v205, v50, 1, 6
	v_lshl_or_b32 v255, v205, 4, v255
	v_add_u32_e32 v255, 0x14000, v255
	v_mbcnt_lo_u32_b32 v205, -1, 0
	v_mbcnt_hi_u32_b32 v205, -1, v205
	v_lshlrev_b32_e32 v205, 4, v205
	v_add_u32_e32 v205, 0x14000, v205
	s_waitcnt vmcnt(0)
	ds_write_b128 v255, v[244:247]
	ds_write_b128 v255, v[248:251] offset:8192
	s_waitcnt lgkmcnt(0)
	s_barrier
; #define GAS __attribute__((address_space(1)))
; template <bool X8>
; __device__ __forceinline__ void ln_router_phase(Frame& F, int layer) {
;     ...
;         const int tt4 = w & 3, kh = w >> 2;
;         u32x4 xr[4], wq[4];
;         const GAS bf16_t* wrb = (const GAS bf16_t*)(F.ws + WS_WRB) + (size_t)layer * D_MODEL * N_EXPERTS;
; #pragma unroll
;         for (int j = 0; j < 4; ++j) { const int idx = tid + 512 * j, row = idx >> 5, c8 = idx & 31; xr[j] = *(const GAS u32x4*)(X1B + (size_t)(tok0 + row) * D_MODEL + 8 * c8); }
; #pragma unroll
;         for (int j = 0; j < 4; ++j) { const int idx = tid + 512 * j, row = idx >> 3, c8 = idx & 7; wq[j] = *(const GAS u32x4*)(wrb + (size_t)row * N_EXPERTS + 8 * c8); }
; #pragma unroll 1
;         for (int ke = 0; ke < 8; ++ke) { const int k1 = 256 * (ke + 1);
; #pragma unroll
;             for (int j = 0; j < 4; ++j) { const int idx = tid + 512 * j, row = idx >> 5, c8 = idx & 31; *(LAS u32x4*)(XSb + row * XROW + c8 * 16) = xr[j]; }
; #pragma unroll
;             for (int j = 0; j < 4; ++j) { const int idx = tid + 512 * j, row = idx >> 3, c8 = idx & 7; *(LAS u32x4*)(WSb + row * WROW + c8 * 16) = wq[j]; }
;             LDS_BARRIER();
;             if (ke < 7) {
; #pragma unroll
;                 for (int j = 0; j < 4; ++j) { const int idx = tid + 512 * j, row = idx >> 5, c8 = idx & 31; xr[j] = *(const GAS u32x4*)(X1B + (size_t)(tok0 + row) * D_MODEL + k1 + 8 * c8); }
; #pragma unroll
;                 for (int j = 0; j < 4; ++j) { const int idx = tid + 512 * j, row = idx >> 3, c8 = idx & 7; wq[j] = *(const GAS u32x4*)(wrb + (size_t)(k1 + row) * N_EXPERTS + 8 * c8); }
;             }
;             { const unsigned wsb = (unsigned)(size_t)WSb; const int q = i >> 2, p4 = i & 3;
; #pragma unroll
;               for (int ks = 0; ks < 4; ++ks) { const int kk0 = 128 * kh + 32 * ks;
;                 const bf16x8 a = *(const LAS bf16x8*)(XSb + (tt4 * 16 + i) * XROW + (kk0 + 8 * g) * 2);
;                 s16x4 lo4[4], hi4[4];
;                 tr_read4x2<32>(lo4, hi4, wsb + (kk0 + 8 * g + q) * WROW + 8 * p4, wsb + (kk0 + 8 * g + 4 + q) * WROW + 8 * p4);
; #pragma unroll
;                 for (int nb = 0; nb < 4; ++nb) dacc[nb] = mfma16(a, TRCAT(lo4[nb], hi4[nb]), dacc[nb]); } }
;             LDS_BARRIER();
;         }
; #pragma unroll
;         for (int nb = 0; nb < 4; ++nb)
; #pragma unroll
	v_or_b32_e32 v54, 0x1800, v54
	v_mul_lo_u32 v7, v177, s17
	v_mul_lo_u32 v11, v178, s17
	v_mul_lo_u32 v15, v179, s17
	v_mul_lo_u32 v28, v180, s17
	v_mul_lo_u32 v29, v64, s6
	v_mul_lo_u32 v6, v6, s6
	v_mul_lo_u32 v10, v10, s6
	v_mul_lo_u32 v14, v14, s6
	v_add_u32_e32 v184, v31, v22
	v_add_u32_e32 v185, v31, v23
	v_lshlrev_b32_e32 v31, 1, v21
	v_lshlrev_b32_e32 v21, 8, v24
	s_add_i32 s72, s22, s3
	v_or_b32_e32 v16, v16, v2
	s_mov_b64 s[20:21], 0x1d258000
	v_or_b32_e32 v12, v12, v2
	v_or_b32_e32 v8, v8, v2
	v_or_b32_e32 v4, v4, v2
	v_and_b32_e32 v2, 31, v50
	v_mov_b32_e32 v3, 0x31300200
	s_mov_b64 s[70:71], 0x2000
	v_lshlrev_b32_e32 v52, 3, v1
	v_lshl_add_u32 v174, v50, 5, s1
	v_cmp_gt_i32_e64 s[4:5], 64, v50
	v_lshl_add_u32 v175, v50, 2, s1
	v_lshlrev_b64 v[60:61], v26, s[12:13]
	v_lshl_add_u64 v[80:81], s[10:11], 0, v[54:55]
	v_lshl_add_u64 v[82:83], s[8:9], 0, v[54:55]
	v_cmp_lt_u32_e64 s[6:7], 7, v1
	v_cmp_lt_u32_e64 s[8:9], 15, v1
	v_cmp_lt_u32_e64 s[10:11], 23, v1
	v_cmp_lt_u32_e64 s[12:13], 31, v1
	v_cmp_lt_u32_e64 s[14:15], 39, v1
	v_cmp_lt_u32_e64 s[16:17], 47, v1
	v_cmp_eq_u32_e64 s[18:19], 56, v26
	s_or_b32 s74, s72, 1
	s_lshl_b32 s24, s0, 6
	v_lshlrev_b32_e32 v92, 4, v1
	v_lshl_add_u64 v[94:95], v[16:17], 0, s[20:21]
	v_lshl_add_u64 v[96:97], v[12:13], 0, s[20:21]
	v_lshl_add_u64 v[98:99], v[8:9], 0, s[20:21]
	v_lshl_add_u64 v[100:101], v[4:5], 0, s[20:21]
	v_lshl_or_b32 v54, v2, 4, v3
	v_add_u32_e32 v102, s22, v180
	v_add_u32_e32 v104, s22, v179
	v_add_u32_e32 v106, s22, v178
	v_add_u32_e32 v108, s22, v177
	s_mov_b32 s25, 0x1d300000
	v_mov_b32_e32 v188, 0x3727c5ac
	s_mov_b32 s33, 0x800000
	s_mov_b32 s50, 0x31300000
	s_mov_b32 s51, 0x71f00000
	s_mov_b64 s[76:77], 0x1000
	v_add_u32_e32 v189, v18, v7
	v_add_u32_e32 v190, v18, v11
	v_add_u32_e32 v191, v18, v15
	v_add_u32_e32 v192, v18, v28
	v_add_u32_e32 v193, v19, v29
	v_add_u32_e32 v194, v19, v6
	v_add_u32_e32 v195, v19, v10
	v_add_u32_e32 v196, v19, v14
	v_add_u32_e32 v197, v20, v30
	v_add_u32_e32 v198, v20, v32
	v_add_u32_e32 v199, v20, v33
	v_add_u32_e32 v200, v20, v31
	s_mov_b64 s[78:79], 0x8000
	s_mov_b64 s[80:81], 0x200
	v_add_u32_e32 v201, v25, v21
	s_mov_b32 s56, 0xbfb8aa3b
	s_mov_b32 s57, 0x42ce8ed0
	s_mov_b32 s84, 0xc2b17218
	v_mov_b32_e32 v202, 1
	v_mov_b32_e32 v203, 0x7f800000
	v_mov_b32_e32 v204, 0xff800000
	s_branch .LBB0_2872

; #define GAS __attribute__((address_space(1)))
; template <bool X8>
; __device__ __forceinline__ void ln_router_phase(Frame& F, int layer) {
;     ...
;         for (int pr = 0; pr < 4; ++pr) {
;             f32x4 ys[2][4][2];
; #pragma unroll
;             for (int tt = 0; tt < 2; ++tt) { const size_t token = (size_t)(tok0 + 8 * w + 2 * pr + tt);
;                 const GAS u32x4* rp = (const GAS u32x4*)(R + token * D_MODEL) + lane;
; #pragma unroll
;                 for (int j = 0; j < 4; ++j) { const u32x4 r = rp[64 * j]; ys[tt][j][0] = (f32x4){bflo(r.x), bfhi(r.x), bflo(r.y), bfhi(r.y)}; ys[tt][j][1] = (f32x4){bflo(r.z), bfhi(r.z), bflo(r.w), bfhi(r.w)}; } }
; #pragma unroll
;             for (int tt = 0; tt < 2; ++tt) { const size_t token = (size_t)(tok0 + 8 * w + 2 * pr + tt); float s = 0.f;
; #pragma unroll
;                 for (int j = 0; j < 4; ++j)
; #pragma unroll
;                     for (int h = 0; h < 2; ++h) s += (ys[tt][j][h][0] + ys[tt][j][h][1]) + (ys[tt][j][h][2] + ys[tt][j][h][3]);
;                 const float mean = wave_sum(s) * (1.0f / D_MODEL); float s2 = 0.f;
.LBB0_2873:
	v_lshl_add_u64 v[26:27], s[62:63], 0, v[24:25]
	v_lshl_add_u64 v[28:29], s[62:63], 0, v[20:21]
	v_add_co_u32_e32 v46, vcc, 0x1d300000, v26
	v_add_co_u32_e64 v48, s[20:21], s25, v28
	s_nop 0
	v_addc_co_u32_e32 v47, vcc, 0, v27, vcc
	v_addc_co_u32_e64 v49, s[20:21], 0, v29, s[20:21]
	ds_read_b128 v[2:5], v205 offset:1024
	ds_read_b128 v[10:13], v205 offset:0
	ds_read_b128 v[6:9], v205 offset:9216
	ds_read_b128 v[14:17], v205 offset:8192
	global_load_dwordx4 v[132:135], v[48:49], off offset:1024
	global_load_dwordx4 v[136:139], v[48:49], off offset:2048
	global_load_dwordx4 v[42:45], v[48:49], off offset:3072
	global_load_dwordx4 v[140:143], v[48:49], off
	global_load_dwordx4 v[206:209], v[46:47], off offset:1024
	global_load_dwordx4 v[210:213], v[46:47], off offset:2048
	global_load_dwordx4 v[214:217], v[46:47], off offset:3072
	global_load_dwordx4 v[218:221], v[46:47], off
	v_add_co_u32_e64 v130, s[20:21], s50, v26
	v_lshl_add_u64 v[38:39], s[62:63], 0, v[22:23]
	s_nop 0
	v_addc_co_u32_e64 v131, s[20:21], 0, v27, s[20:21]
	v_add_co_u32_e64 v128, s[20:21], s51, v38
	v_lshl_add_u64 v[40:41], s[62:63], 0, v[18:19]
	s_nop 0
	v_addc_co_u32_e64 v129, s[20:21], 0, v39, s[20:21]
	v_add_co_u32_e64 v28, s[20:21], s50, v28
	v_mov_b32_e32 v32, 0
	s_nop 0
	v_addc_co_u32_e64 v29, s[20:21], 0, v29, s[20:21]
	v_add_co_u32_e64 v38, s[20:21], s51, v40
	v_mov_b32_e32 v33, 0
	s_nop 0
	v_addc_co_u32_e64 v39, s[20:21], 0, v41, s[20:21]
	v_mov_b32_e32 v36, 0
	v_mov_b32_e32 v37, 0
	v_mov_b32_e32 v34, 0
	v_mov_b32_e32 v35, 0
	v_mov_b32_e32 v30, 0
	v_mov_b32_e32 v31, 0
	v_mov_b32_e32 v124, 0
	v_mov_b32_e32 v125, 0
	s_add_i32 s22, s22, -1
	v_lshl_add_u64 v[18:19], v[18:19], 0, s[76:77]
	v_lshl_add_u64 v[20:21], v[20:21], 0, s[70:71]
	v_lshl_add_u64 v[22:23], v[22:23], 0, s[76:77]
	v_lshl_add_u64 v[24:25], v[24:25], 0, s[70:71]
	s_cmp_eq_u32 s22, 0
	s_waitcnt vmcnt(7)
	v_lshlrev_b32_e32 v120, 16, v134
	v_and_b32_e32 v121, 0xffff0000, v134
	v_lshlrev_b32_e32 v122, 16, v135
	v_and_b32_e32 v123, 0xffff0000, v135
	s_waitcnt vmcnt(6)
	v_lshlrev_b32_e32 v110, 16, v136
	v_and_b32_e32 v114, 0xffff0000, v136
	s_waitcnt vmcnt(4)
	v_lshlrev_b32_e32 v159, 16, v140
	v_lshlrev_b32_e32 v158, 16, v142
	v_and_b32_e32 v157, 0xffff0000, v140
	v_and_b32_e32 v156, 0xffff0000, v142
	v_lshlrev_b32_e32 v127, 16, v133
	v_lshlrev_b32_e32 v126, 16, v132
	v_and_b32_e32 v151, 0xffff0000, v133
	v_and_b32_e32 v150, 0xffff0000, v132
	v_lshlrev_b32_e32 v118, 16, v138
	v_and_b32_e32 v146, 0xffff0000, v138
	s_waitcnt vmcnt(3)
	v_lshlrev_b32_e32 v166, 16, v208
	v_and_b32_e32 v167, 0xffff0000, v208
	v_lshlrev_b32_e32 v168, 16, v209
	v_and_b32_e32 v169, 0xffff0000, v209
	s_waitcnt vmcnt(2)
	v_lshlrev_b32_e32 v152, 16, v210
	v_and_b32_e32 v160, 0xffff0000, v210
	v_lshlrev_b32_e32 v154, 16, v211
	v_and_b32_e32 v162, 0xffff0000, v211
	s_waitcnt vmcnt(1)
	v_lshlrev_b32_e32 v132, 16, v214
	v_and_b32_e32 v133, 0xffff0000, v214
	v_lshlrev_b32_e32 v134, 16, v215
	v_and_b32_e32 v135, 0xffff0000, v215
	v_lshlrev_b32_e32 v136, 16, v216
	v_and_b32_e32 v140, 0xffff0000, v216
	v_lshlrev_b32_e32 v138, 16, v217
	v_and_b32_e32 v142, 0xffff0000, v217
	s_waitcnt vmcnt(0) lgkmcnt(0)
	v_lshlrev_b32_e32 v209, 16, v218
	v_lshlrev_b32_e32 v208, 16, v220
	v_and_b32_e32 v211, 0xffff0000, v218
	v_and_b32_e32 v210, 0xffff0000, v220
	v_lshlrev_b32_e32 v215, 16, v219
	v_lshlrev_b32_e32 v214, 16, v221
	v_and_b32_e32 v217, 0xffff0000, v219
	v_and_b32_e32 v216, 0xffff0000, v221
	v_lshlrev_b32_e32 v26, 16, v42
	v_and_b32_e32 v27, 0xffff0000, v42
	v_lshlrev_b32_e32 v40, 16, v43
	v_and_b32_e32 v41, 0xffff0000, v43
	v_lshlrev_b32_e32 v219, 16, v207
	v_lshlrev_b32_e32 v218, 16, v206
	v_and_b32_e32 v207, 0xffff0000, v207
	v_and_b32_e32 v206, 0xffff0000, v206
	v_pk_add_f32 v[228:229], v[208:209], v[210:211]
	v_pk_add_f32 v[230:231], v[214:215], v[216:217]
	v_lshlrev_b32_e32 v42, 16, v44
	v_and_b32_e32 v46, 0xffff0000, v44
	v_lshlrev_b32_e32 v149, 16, v141
	v_lshlrev_b32_e32 v148, 16, v143
	v_and_b32_e32 v145, 0xffff0000, v141
	v_and_b32_e32 v144, 0xffff0000, v143
	v_add_f32_e32 v43, v26, v27
	v_add_f32_e32 v47, v40, v41
	v_pk_add_f32 v[232:233], v[218:219], v[206:207]
	v_pk_add_f32 v[228:229], v[228:229], v[230:231]
	v_pk_add_f32 v[220:221], v[158:159], v[156:157]
	v_pk_add_f32 v[222:223], v[148:149], v[144:145]
	v_pk_add_f32 v[224:225], v[126:127], v[150:151]
	v_pk_add_f32 v[236:237], v[42:43], v[46:47]
	v_pk_add_f32 v[230:231], v[232:233], v[232:233] op_sel_hi:[0,1]
	v_add_f32_e32 v47, 0, v229
	v_add_f32_e32 v153, v166, v167
	v_add_f32_e32 v161, v168, v169
	v_pk_add_f32 v[220:221], v[220:221], v[222:223]
	v_pk_add_f32 v[222:223], v[224:225], v[224:225] op_sel_hi:[0,1]
	v_mov_b32_e32 v155, v231
	v_add_f32_e32 v163, v228, v47
	v_lshlrev_b32_e32 v165, 16, v213
	v_lshlrev_b32_e32 v164, 16, v212
	v_and_b32_e32 v213, 0xffff0000, v213
	v_and_b32_e32 v212, 0xffff0000, v212
	v_pk_add_f32 v[232:233], v[152:153], v[160:161]
	v_add_f32_e32 v43, 0, v221
	v_mov_b32_e32 v113, v223
	v_pk_add_f32 v[222:223], v[154:155], v[162:163]
	v_lshlrev_b32_e32 v112, 16, v137
	v_and_b32_e32 v116, 0xffff0000, v137
	v_add_f32_e32 v111, v120, v121
	v_add_f32_e32 v115, v122, v123
	v_pk_add_f32 v[234:235], v[164:165], v[212:213]
	v_add_f32_e32 v117, v220, v43
	v_pk_add_f32 v[222:223], v[232:233], v[222:223]
	v_lshlrev_b32_e32 v119, 16, v139
	v_and_b32_e32 v147, 0xffff0000, v139
	v_pk_add_f32 v[224:225], v[110:111], v[114:115]
	v_pk_add_f32 v[234:235], v[234:235], v[234:235] op_sel_hi:[0,1]
	v_pk_add_f32 v[220:221], v[112:113], v[116:117]
	v_pk_add_f32 v[222:223], v[222:223], v[222:223] op_sel_hi:[0,1]
	v_pk_add_f32 v[226:227], v[118:119], v[146:147]
	v_add_f32_e32 v137, v132, v133
	v_add_f32_e32 v141, v134, v135
	v_mov_b32_e32 v139, v235
	v_pk_add_f32 v[220:221], v[224:225], v[220:221]
	v_mov_b32_e32 v143, v223
	v_pk_add_f32 v[226:227], v[226:227], v[226:227] op_sel_hi:[0,1]
	v_pk_add_f32 v[238:239], v[136:137], v[140:141]
	v_pk_add_f32 v[220:221], v[220:221], v[220:221] op_sel_hi:[0,1]
	v_pk_add_f32 v[222:223], v[138:139], v[142:143]
	v_lshlrev_b32_e32 v44, 16, v45
	v_and_b32_e32 v48, 0xffff0000, v45
	v_mov_b32_e32 v45, v227
	v_mov_b32_e32 v49, v221
	v_pk_add_f32 v[222:223], v[238:239], v[222:223]
	v_pk_add_f32 v[220:221], v[44:45], v[48:49]
	v_add_f32_e32 v45, v222, v223
	ds_bpermute_b32 v49, v53, v45
	v_pk_add_f32 v[220:221], v[236:237], v[220:221]
	s_waitcnt lgkmcnt(0)
; __device__ __forceinline__ float wave_sum(float v) {
; #pragma unroll
;     for (int o = 1; o < 64; o <<= 1) v += __shfl_xor(v, o);
;     return v;
; }
; template <bool X8>
; __device__ __forceinline__ void ln_router_phase(Frame& F, int layer) {
;     ...
;             for (int tt = 0; tt < 2; ++tt) { const size_t token = (size_t)(tok0 + 8 * w + 2 * pr + tt); float s = 0.f;
; #pragma unroll
;                 for (int j = 0; j < 4; ++j)
; #pragma unroll
;                     for (int h = 0; h < 2; ++h) s += (ys[tt][j][h][0] + ys[tt][j][h][1]) + (ys[tt][j][h][2] + ys[tt][j][h][3]);
;                 const float mean = wave_sum(s) * (1.0f / D_MODEL); float s2 = 0.f;
; #pragma unroll
;                 for (int j = 0; j < 4; ++j)
; #pragma unroll
;                     for (int h = 0; h < 2; ++h) { ys[tt][j][h] = ys[tt][j][h] - mean; s2 += (ys[tt][j][h][0] * ys[tt][j][h][0] + ys[tt][j][h][1] * ys[tt][j][h][1]) + (ys[tt][j][h][2] * ys[tt][j][h][2] + ys[tt][j][h][3] * ys[tt][j][h][3]); }
;                 const float rstd = rsqrtf(wave_sum(s2) * (1.0f / D_MODEL) + LN_EPS);
	v_add_f32_e32 v45, v45, v49
	ds_bpermute_b32 v49, v93, v45
	v_add_f32_e32 v43, v220, v221
	ds_bpermute_b32 v47, v53, v43
	s_waitcnt lgkmcnt(1)
	v_add_f32_e32 v45, v45, v49
	ds_bpermute_b32 v49, v170, v45
	s_waitcnt lgkmcnt(1)
	v_add_f32_e32 v43, v43, v47
	ds_bpermute_b32 v47, v93, v43
	s_waitcnt lgkmcnt(1)
	v_add_f32_e32 v45, v45, v49
	ds_bpermute_b32 v49, v171, v45
	s_waitcnt lgkmcnt(1)
	v_add_f32_e32 v43, v43, v47
	ds_bpermute_b32 v47, v170, v43
	s_waitcnt lgkmcnt(1)
	v_add_f32_e32 v45, v45, v49
	ds_bpermute_b32 v49, v172, v45
	s_waitcnt lgkmcnt(1)
	v_add_f32_e32 v43, v43, v47
	ds_bpermute_b32 v47, v171, v43
	s_waitcnt lgkmcnt(1)
	v_add_f32_e32 v45, v45, v49
	ds_bpermute_b32 v49, v173, v45
	s_waitcnt lgkmcnt(1)
	v_add_f32_e32 v43, v43, v47
	ds_bpermute_b32 v47, v172, v43
	s_waitcnt lgkmcnt(1)
	v_add_f32_e32 v45, v45, v49
	v_fmac_f32_e32 v217, 0xba000000, v45
	v_fmac_f32_e32 v215, 0xba000000, v45
	v_fmac_f32_e32 v211, 0xba000000, v45
	v_fmac_f32_e32 v209, 0xba000000, v45
	v_fmac_f32_e32 v216, 0xba000000, v45
	v_fmac_f32_e32 v214, 0xba000000, v45
	v_fmac_f32_e32 v210, 0xba000000, v45
	v_fmac_f32_e32 v208, 0xba000000, v45
	v_fmac_f32_e32 v206, 0xba000000, v45
	v_fmac_f32_e32 v207, 0xba000000, v45
	v_fmac_f32_e32 v219, 0xba000000, v45
	v_fmac_f32_e32 v218, 0xba000000, v45
	v_mov_b32_e32 v220, v208
	v_mov_b32_e32 v221, v210
	v_mov_b32_e32 v222, v209
	v_mov_b32_e32 v223, v211
	v_mov_b32_e32 v224, v209
	v_mov_b32_e32 v225, v208
	v_mov_b32_e32 v208, v211
	v_mov_b32_e32 v209, v210
	v_mov_b32_e32 v210, v214
	v_mov_b32_e32 v211, v216
	v_mov_b32_e32 v226, v215
	v_mov_b32_e32 v227, v217
	v_mov_b32_e32 v228, v215
	v_mov_b32_e32 v229, v214
	v_mov_b32_e32 v214, v217
	v_mov_b32_e32 v215, v216
	v_mov_b32_e32 v216, v219
	v_mov_b32_e32 v217, v207
	v_mov_b32_e32 v219, v206
	v_pk_mul_f32 v[208:209], v[208:209], v[208:209]
	v_pk_mul_f32 v[214:215], v[214:215], v[214:215]
	v_pk_mul_f32 v[236:237], v[216:217], v[216:217]
	v_pk_mul_f32 v[238:239], v[218:219], v[218:219]
	v_fmac_f32_e32 v166, 0xba000000, v45
	v_fmac_f32_e32 v168, 0xba000000, v45
	v_pk_fma_f32 v[208:209], v[224:225], v[224:225], v[208:209]
	v_pk_fma_f32 v[214:215], v[228:229], v[228:229], v[214:215]
	v_pk_mov_b32 v[224:225], v[238:239], v[236:237] op_sel:[1,0]
	v_mov_b32_e32 v239, v237
	v_fmac_f32_e32 v167, 0xba000000, v45
	v_fmac_f32_e32 v169, 0xba000000, v45
	v_fmac_f32_e32 v212, 0xba000000, v45
	v_fmac_f32_e32 v213, 0xba000000, v45
	v_fmac_f32_e32 v165, 0xba000000, v45
	v_mul_f32_e32 v206, v166, v166
	v_mul_f32_e32 v230, v168, v168
	v_pk_add_f32 v[208:209], v[208:209], v[214:215]
	v_pk_add_f32 v[214:215], v[224:225], v[238:239]
	v_fmac_f32_e32 v162, 0xba000000, v45
	v_fmac_f32_e32 v154, 0xba000000, v45
	v_fmac_f32_e32 v160, 0xba000000, v45
	v_fmac_f32_e32 v152, 0xba000000, v45
	v_fmac_f32_e32 v164, 0xba000000, v45
	v_mov_b32_e32 v232, v165
	v_mov_b32_e32 v233, v213
	v_mov_b32_e32 v165, v212
	v_pk_fma_f32 v[206:207], v[166:167], v[166:167], v[206:207] op_sel_hi:[1,1,0]
	v_pk_fma_f32 v[230:231], v[168:169], v[168:169], v[230:231] op_sel_hi:[1,1,0]
	v_pk_add_f32 v[208:209], v[208:209], v[208:209] op_sel_hi:[0,1]
	v_pk_add_f32 v[214:215], v[214:215], v[214:215] op_sel_hi:[0,1]
	v_pk_mul_f32 v[240:241], v[232:233], v[232:233]
	v_pk_mul_f32 v[242:243], v[164:165], v[164:165]
	v_mul_f32_e32 v206, v152, v152
	v_mul_f32_e32 v230, v160, v160
	v_mul_f32_e32 v214, v154, v154
	v_mul_f32_e32 v208, v162, v162
	v_fmac_f32_e32 v132, 0xba000000, v45
	v_fmac_f32_e32 v134, 0xba000000, v45
	v_pk_mov_b32 v[228:229], v[242:243], v[240:241] op_sel:[1,0]
	v_mov_b32_e32 v243, v241
	v_pk_add_f32 v[206:207], v[206:207], v[230:231]
	v_pk_add_f32 v[208:209], v[214:215], v[208:209]
	s_waitcnt lgkmcnt(0)
	v_add_f32_e32 v43, v43, v47
	v_fmac_f32_e32 v133, 0xba000000, v45
	v_fmac_f32_e32 v135, 0xba000000, v45
	v_mul_f32_e32 v212, v132, v132
	v_mul_f32_e32 v234, v134, v134
	v_pk_add_f32 v[224:225], v[228:229], v[242:243]
	v_pk_add_f32 v[206:207], v[206:207], v[208:209]
	ds_bpermute_b32 v47, v173, v43
	v_fmac_f32_e32 v142, 0xba000000, v45
	v_fmac_f32_e32 v138, 0xba000000, v45
	v_fmac_f32_e32 v140, 0xba000000, v45
	v_fmac_f32_e32 v136, 0xba000000, v45
	v_pk_fma_f32 v[212:213], v[132:133], v[132:133], v[212:213] op_sel_hi:[1,1,0]
	v_pk_fma_f32 v[234:235], v[134:135], v[134:135], v[234:235] op_sel_hi:[1,1,0]
	v_pk_add_f32 v[224:225], v[224:225], v[224:225] op_sel_hi:[0,1]
	v_pk_add_f32 v[206:207], v[206:207], v[206:207] op_sel_hi:[0,1]
	v_mul_f32_e32 v212, v136, v136
	v_mul_f32_e32 v234, v140, v140
	v_mul_f32_e32 v224, v138, v138
	v_mul_f32_e32 v206, v142, v142
	v_pk_add_f32 v[212:213], v[212:213], v[234:235]
	v_pk_add_f32 v[206:207], v[224:225], v[206:207]
	s_waitcnt lgkmcnt(0)
	v_add_f32_e32 v43, v43, v47
	v_pk_add_f32 v[206:207], v[212:213], v[206:207]
	v_mov_b32_e32 v153, v160
	v_add_f32_e32 v45, v206, v207
	ds_bpermute_b32 v47, v53, v45
	v_mov_b32_e32 v155, v162
	v_mov_b32_e32 v137, v140
	v_mov_b32_e32 v139, v142
	v_fmac_f32_e32 v145, 0xba000000, v43
	s_waitcnt lgkmcnt(0)
	v_add_f32_e32 v45, v45, v47
	ds_bpermute_b32 v47, v93, v45
	v_fmac_f32_e32 v149, 0xba000000, v43
	v_fmac_f32_e32 v157, 0xba000000, v43
	v_fmac_f32_e32 v159, 0xba000000, v43
	v_fmac_f32_e32 v144, 0xba000000, v43
	s_waitcnt lgkmcnt(0)
	v_add_f32_e32 v45, v45, v47
	ds_bpermute_b32 v47, v170, v45
	v_fmac_f32_e32 v148, 0xba000000, v43
	v_fmac_f32_e32 v156, 0xba000000, v43
	v_fmac_f32_e32 v158, 0xba000000, v43
	v_fmac_f32_e32 v150, 0xba000000, v43
	s_waitcnt lgkmcnt(0)
	v_add_f32_e32 v45, v45, v47
	ds_bpermute_b32 v47, v171, v45
	v_fmac_f32_e32 v151, 0xba000000, v43
	v_fmac_f32_e32 v127, 0xba000000, v43
	v_fmac_f32_e32 v126, 0xba000000, v43
	v_fmac_f32_e32 v120, 0xba000000, v43
	s_waitcnt lgkmcnt(0)
; #define GAS __attribute__((address_space(1)))
; __device__ __forceinline__ unsigned cvt_pk_bf16(float lo, float hi) { unsigned r; asm volatile("v_cvt_pk_bf16_f32 %0, %1, %2" : "=v"(r) : "v"(lo), "v"(hi)); return r; }
; template <bool X8>
; __device__ __forceinline__ void ln_router_phase(Frame& F, int layer) {
;     ...
;                 const float rstd = rsqrtf(wave_sum(s2) * (1.0f / D_MODEL) + LN_EPS);
; #pragma unroll
;                 for (int j = 0; j < 4; ++j) { const int c = 8 * lane + 512 * j;
;                     const f32x4 y0 = ys[tt][j][0] * rstd * *(const GAS f32x4*)(g1 + c) + *(const GAS f32x4*)(b1 + c), y1 = ys[tt][j][1] * rstd * *(const GAS f32x4*)(g1 + c + 4) + *(const GAS f32x4*)(b1 + c + 4);
;                     u32x4 o; o.x = cvt_pk_bf16(y0[0], y0[1]); o.y = cvt_pk_bf16(y0[2], y0[3]); o.z = cvt_pk_bf16(y1[0], y1[1]); o.w = cvt_pk_bf16(y1[2], y1[3]);
;                     *(GAS u32x4*)(X1B + token * D_MODEL + c) = o;
;                     if constexpr (X8) { u32x2 w8; int q8 = __builtin_amdgcn_cvt_pk_fp8_f32(y0[0], y0[1], 0, false); q8 = __builtin_amdgcn_cvt_pk_fp8_f32(y0[2], y0[3], q8, true); w8.x = (unsigned)q8;
;                         q8 = __builtin_amdgcn_cvt_pk_fp8_f32(y1[0], y1[1], 0, false); q8 = __builtin_amdgcn_cvt_pk_fp8_f32(y1[2], y1[3], q8, true); w8.y = (unsigned)q8;
;                         *(GAS u32x2*)(X1B8 + token * D_MODEL + c) = w8; } }
	v_add_f32_e32 v45, v45, v47
	ds_bpermute_b32 v47, v172, v45
	v_fmac_f32_e32 v122, 0xba000000, v43
	v_fmac_f32_e32 v121, 0xba000000, v43
	v_fmac_f32_e32 v123, 0xba000000, v43
	v_fmac_f32_e32 v146, 0xba000000, v43
	s_waitcnt lgkmcnt(0)
	v_add_f32_e32 v45, v45, v47
	ds_bpermute_b32 v47, v173, v45
	v_fmac_f32_e32 v147, 0xba000000, v43
	v_fmac_f32_e32 v119, 0xba000000, v43
	v_fmac_f32_e32 v116, 0xba000000, v43
	v_fmac_f32_e32 v112, 0xba000000, v43
	s_waitcnt lgkmcnt(0)
	v_add_f32_e32 v45, v45, v47
	v_fmamk_f32 v45, v45, 0x3a000000, v188
	v_mul_f32_e32 v47, 0x4b800000, v45
	v_cmp_gt_f32_e32 vcc, s33, v45
	v_fmac_f32_e32 v114, 0xba000000, v43
	v_fmac_f32_e32 v110, 0xba000000, v43
	v_cndmask_b32_e32 v45, v45, v47, vcc
	v_rsq_f32_e32 v45, v45
	v_fmac_f32_e32 v118, 0xba000000, v43
	v_fmac_f32_e32 v26, 0xba000000, v43
	v_fmac_f32_e32 v40, 0xba000000, v43
	v_mul_f32_e32 v47, 0x45800000, v45
	v_cndmask_b32_e32 v206, v45, v47, vcc
	v_pk_mul_f32 v[208:209], v[222:223], v[206:207] op_sel_hi:[1,0]
	v_pk_mul_f32 v[214:215], v[220:221], v[206:207] op_sel_hi:[1,0]
	v_pk_fma_f32 v[10:11], v[10:11], v[208:209], v[14:15]
	v_pk_fma_f32 v[6:7], v[2:3], v[214:215], v[6:7]
	v_cvt_pk_fp8_f32 v32, v10, v11
	v_cvt_pk_fp8_f32 v33, v6, v7
	v_pk_mul_f32 v[212:213], v[226:227], v[206:207] op_sel_hi:[1,0]
	v_pk_mul_f32 v[210:211], v[210:211], v[206:207] op_sel_hi:[1,0]
	v_pk_fma_f32 v[12:13], v[12:13], v[212:213], v[16:17]
	v_pk_fma_f32 v[8:9], v[4:5], v[210:211], v[8:9]
	v_cvt_pk_fp8_f32 v32, v12, v13 op_sel:[0,0,1]
	v_cvt_pk_fp8_f32 v33, v8, v9 op_sel:[0,0,1]
	v_cvt_pk_bf16_f32 v2, v10, v11
	v_cvt_pk_bf16_f32 v3, v12, v13
	v_cvt_pk_bf16_f32 v4, v6, v7
	v_cvt_pk_bf16_f32 v5, v8, v9
	global_store_dwordx4 v[130:131], v[2:5], off
	global_store_dwordx2 v[128:129], v[32:33], off
	ds_read_b128 v[2:5], v205 offset:10240
	s_nop 0
	ds_read_b128 v[6:9], v205 offset:2048
	ds_read_b128 v[10:13], v205 offset:3072
	ds_read_b128 v[14:17], v205 offset:11264
	v_pk_mul_f32 v[32:33], v[218:219], v[206:207] op_sel_hi:[1,0]
	v_pk_mul_f32 v[166:167], v[166:167], v[206:207] op_sel_hi:[1,0]
	v_pk_mul_f32 v[208:209], v[216:217], v[206:207] op_sel_hi:[1,0]
	v_pk_mul_f32 v[168:169], v[168:169], v[206:207] op_sel_hi:[1,0]
	v_pk_mul_f32 v[152:153], v[152:153], v[206:207] op_sel_hi:[1,0]
	v_pk_mul_f32 v[160:161], v[164:165], v[206:207] op_sel_hi:[1,0]
	v_pk_mul_f32 v[154:155], v[154:155], v[206:207] op_sel_hi:[1,0]
	v_pk_mul_f32 v[162:163], v[232:233], v[206:207] op_sel_hi:[1,0]
	v_pk_mul_f32 v[132:133], v[132:133], v[206:207] op_sel_hi:[1,0]
	v_pk_mul_f32 v[136:137], v[136:137], v[206:207] op_sel_hi:[1,0]
	v_pk_mul_f32 v[134:135], v[134:135], v[206:207] op_sel_hi:[1,0]
	v_pk_mul_f32 v[138:139], v[138:139], v[206:207] op_sel_hi:[1,0]
	v_mul_f32_e32 v210, v122, v122
	v_mov_b32_e32 v212, v119
	v_mov_b32_e32 v213, v147
	v_mov_b32_e32 v119, v146
	v_fmac_f32_e32 v27, 0xba000000, v43
	v_fmac_f32_e32 v41, 0xba000000, v43
	v_mul_f32_e32 v146, v26, v26
	v_mul_f32_e32 v214, v40, v40
	v_fmac_f32_e32 v48, 0xba000000, v43
	v_fmac_f32_e32 v44, 0xba000000, v43
	v_fmac_f32_e32 v46, 0xba000000, v43
	v_fmac_f32_e32 v42, 0xba000000, v43
	v_pk_fma_f32 v[146:147], v[26:27], v[26:27], v[146:147] op_sel_hi:[1,1,0]
	v_mov_b32_e32 v111, v114
	v_mul_f32_e32 v146, v42, v42
	v_mov_b32_e32 v113, v116
	v_mov_b32_e32 v43, v46
	v_mov_b32_e32 v45, v48
	s_waitcnt lgkmcnt(0)
	v_pk_fma_f32 v[6:7], v[6:7], v[32:33], v[2:3]
	s_nop 0
	v_cvt_pk_fp8_f32 v36, v6, v7
	v_pk_fma_f32 v[10:11], v[10:11], v[166:167], v[14:15]
	v_pk_fma_f32 v[8:9], v[8:9], v[208:209], v[4:5]
	v_cvt_pk_fp8_f32 v37, v10, v11
	v_pk_fma_f32 v[12:13], v[12:13], v[168:169], v[16:17]
	v_cvt_pk_fp8_f32 v36, v8, v9 op_sel:[0,0,1]
	v_cvt_pk_bf16_f32 v2, v6, v7
	v_cvt_pk_fp8_f32 v37, v12, v13 op_sel:[0,0,1]
	v_cvt_pk_bf16_f32 v3, v8, v9
	v_cvt_pk_bf16_f32 v4, v10, v11
	v_cvt_pk_bf16_f32 v5, v12, v13
	global_store_dwordx4 v[130:131], v[2:5], off offset:1024
	global_store_dwordx2 v[128:129], v[36:37], off offset:512
	ds_read_b128 v[2:5], v205 offset:12288
	s_nop 0
	ds_read_b128 v[6:9], v205 offset:4096
	ds_read_b128 v[10:13], v205 offset:5120
	ds_read_b128 v[14:17], v205 offset:13312
	v_mov_b32_e32 v32, v158
	v_mov_b32_e32 v33, v156
	v_mov_b32_e32 v36, v159
	v_mov_b32_e32 v37, v157
	v_mov_b32_e32 v166, v159
	v_mov_b32_e32 v167, v158
	v_mov_b32_e32 v158, v157
	v_mov_b32_e32 v159, v156
	v_mov_b32_e32 v156, v148
	v_mov_b32_e32 v157, v144
	v_mov_b32_e32 v168, v149
	v_mov_b32_e32 v169, v145
	v_mov_b32_e32 v208, v149
	v_mov_b32_e32 v209, v148
	v_mov_b32_e32 v148, v145
	v_mov_b32_e32 v149, v144
	v_mov_b32_e32 v144, v127
	v_mov_b32_e32 v145, v151
	v_mov_b32_e32 v127, v150
	v_pk_mul_f32 v[140:141], v[148:149], v[148:149]
	v_pk_mul_f32 v[142:143], v[144:145], v[144:145]
	v_pk_mul_f32 v[148:149], v[126:127], v[126:127]
	v_pk_fma_f32 v[140:141], v[208:209], v[208:209], v[140:141]
	v_mul_f32_e32 v150, v120, v120
	v_pk_fma_f32 v[150:151], v[120:121], v[120:121], v[150:151] op_sel_hi:[1,1,0]
	s_waitcnt lgkmcnt(0)
; #define GAS __attribute__((address_space(1)))
; __device__ __forceinline__ unsigned cvt_pk_bf16(float lo, float hi) { unsigned r; asm volatile("v_cvt_pk_bf16_f32 %0, %1, %2" : "=v"(r) : "v"(lo), "v"(hi)); return r; }
; template <bool X8>
; __device__ __forceinline__ void ln_router_phase(Frame& F, int layer) {
;     ...
;                 const float mean = wave_sum(s) * (1.0f / D_MODEL); float s2 = 0.f;
; #pragma unroll
;                 for (int j = 0; j < 4; ++j)
; #pragma unroll
;                     for (int h = 0; h < 2; ++h) { ys[tt][j][h] = ys[tt][j][h] - mean; s2 += (ys[tt][j][h][0] * ys[tt][j][h][0] + ys[tt][j][h][1] * ys[tt][j][h][1]) + (ys[tt][j][h][2] * ys[tt][j][h][2] + ys[tt][j][h][3] * ys[tt][j][h][3]); }
;                 const float rstd = rsqrtf(wave_sum(s2) * (1.0f / D_MODEL) + LN_EPS);
; #pragma unroll
;                 for (int j = 0; j < 4; ++j) { const int c = 8 * lane + 512 * j;
;                     const f32x4 y0 = ys[tt][j][0] * rstd * *(const GAS f32x4*)(g1 + c) + *(const GAS f32x4*)(b1 + c), y1 = ys[tt][j][1] * rstd * *(const GAS f32x4*)(g1 + c + 4) + *(const GAS f32x4*)(b1 + c + 4);
;                     u32x4 o; o.x = cvt_pk_bf16(y0[0], y0[1]); o.y = cvt_pk_bf16(y0[2], y0[3]); o.z = cvt_pk_bf16(y1[0], y1[1]); o.w = cvt_pk_bf16(y1[2], y1[3]);
;                     *(GAS u32x4*)(X1B + token * D_MODEL + c) = o;
;                     if constexpr (X8) { u32x2 w8; int q8 = __builtin_amdgcn_cvt_pk_fp8_f32(y0[0], y0[1], 0, false); q8 = __builtin_amdgcn_cvt_pk_fp8_f32(y0[2], y0[3], q8, true); w8.x = (unsigned)q8;
;                         q8 = __builtin_amdgcn_cvt_pk_fp8_f32(y1[0], y1[1], 0, false); q8 = __builtin_amdgcn_cvt_pk_fp8_f32(y1[2], y1[3], q8, true); w8.y = (unsigned)q8;
;                         *(GAS u32x2*)(X1B8 + token * D_MODEL + c) = w8; } }
	v_pk_fma_f32 v[6:7], v[6:7], v[152:153], v[2:3]
	s_nop 0
	v_cvt_pk_fp8_f32 v34, v6, v7
	v_pk_fma_f32 v[10:11], v[160:161], v[10:11], v[14:15]
	v_pk_fma_f32 v[8:9], v[8:9], v[154:155], v[4:5]
	v_cvt_pk_fp8_f32 v35, v10, v11
	v_pk_fma_f32 v[12:13], v[162:163], v[12:13], v[16:17]
	v_cvt_pk_fp8_f32 v34, v8, v9 op_sel:[0,0,1]
	v_cvt_pk_bf16_f32 v2, v6, v7
	v_cvt_pk_fp8_f32 v35, v12, v13 op_sel:[0,0,1]
	v_cvt_pk_bf16_f32 v3, v8, v9
	v_cvt_pk_bf16_f32 v4, v10, v11
	v_cvt_pk_bf16_f32 v5, v12, v13
	global_store_dwordx4 v[130:131], v[2:5], off offset:2048
	global_store_dwordx2 v[128:129], v[34:35], off offset:1024
	ds_read_b128 v[2:5], v205 offset:14336
	s_nop 0
	ds_read_b128 v[6:9], v205 offset:6144
	ds_read_b128 v[10:13], v205 offset:7168
	ds_read_b128 v[14:17], v205 offset:15360
	v_pk_mul_f32 v[34:35], v[158:159], v[158:159]
	v_pk_mov_b32 v[162:163], v[148:149], v[142:143] op_sel:[1,0]
	v_pk_fma_f32 v[34:35], v[166:167], v[166:167], v[34:35]
	v_mov_b32_e32 v149, v143
	v_pk_add_f32 v[34:35], v[34:35], v[140:141]
	v_pk_add_f32 v[140:141], v[162:163], v[148:149]
	v_pk_fma_f32 v[152:153], v[122:123], v[122:123], v[210:211] op_sel_hi:[1,1,0]
	v_pk_add_f32 v[34:35], v[34:35], v[34:35] op_sel_hi:[0,1]
	v_pk_add_f32 v[140:141], v[140:141], v[140:141] op_sel_hi:[0,1]
	v_pk_mul_f32 v[154:155], v[212:213], v[212:213]
	v_pk_mul_f32 v[158:159], v[118:119], v[118:119]
	v_mul_f32_e32 v150, v110, v110
	v_mul_f32_e32 v152, v114, v114
	v_mul_f32_e32 v140, v112, v112
	v_mul_f32_e32 v34, v116, v116
	v_pk_mov_b32 v[142:143], v[158:159], v[154:155] op_sel:[1,0]
	v_mov_b32_e32 v159, v155
	v_pk_add_f32 v[148:149], v[150:151], v[152:153]
	v_pk_add_f32 v[34:35], v[140:141], v[34:35]
	v_pk_add_f32 v[142:143], v[142:143], v[158:159]
	v_pk_add_f32 v[34:35], v[148:149], v[34:35]
	v_pk_fma_f32 v[160:161], v[40:41], v[40:41], v[214:215] op_sel_hi:[1,1,0]
	v_pk_add_f32 v[142:143], v[142:143], v[142:143] op_sel_hi:[0,1]
	v_pk_add_f32 v[34:35], v[34:35], v[34:35] op_sel_hi:[0,1]
	v_mul_f32_e32 v160, v46, v46
	v_mul_f32_e32 v142, v44, v44
	v_mul_f32_e32 v34, v48, v48
	v_pk_add_f32 v[146:147], v[146:147], v[160:161]
	v_pk_add_f32 v[34:35], v[142:143], v[34:35]
	s_waitcnt lgkmcnt(0)
	v_pk_fma_f32 v[6:7], v[132:133], v[6:7], v[2:3]
	s_nop 0
	v_cvt_pk_fp8_f32 v30, v6, v7
	v_pk_fma_f32 v[10:11], v[136:137], v[10:11], v[14:15]
	v_pk_fma_f32 v[8:9], v[134:135], v[8:9], v[4:5]
	v_cvt_pk_fp8_f32 v31, v10, v11
	v_pk_fma_f32 v[12:13], v[138:139], v[12:13], v[16:17]
	v_cvt_pk_fp8_f32 v30, v8, v9 op_sel:[0,0,1]
	v_cvt_pk_bf16_f32 v2, v6, v7
	v_cvt_pk_fp8_f32 v31, v12, v13 op_sel:[0,0,1]
	v_cvt_pk_bf16_f32 v3, v8, v9
	v_cvt_pk_bf16_f32 v4, v10, v11
	v_cvt_pk_bf16_f32 v5, v12, v13
	global_store_dwordx4 v[130:131], v[2:5], off offset:3072
	global_store_dwordx2 v[128:129], v[30:31], off offset:1536
	ds_read_b128 v[2:5], v205 offset:8192
	s_nop 0
	ds_read_b128 v[6:9], v205 offset:0
	ds_read_b128 v[10:13], v205 offset:1024
	ds_read_b128 v[14:17], v205 offset:9216
	v_pk_add_f32 v[34:35], v[146:147], v[34:35]
	s_nop 0
	v_add_f32_e32 v30, v34, v35
	ds_bpermute_b32 v31, v53, v30
	s_waitcnt lgkmcnt(0)
	v_add_f32_e32 v30, v30, v31
	ds_bpermute_b32 v31, v93, v30
	s_waitcnt lgkmcnt(0)
	v_add_f32_e32 v30, v30, v31
	ds_bpermute_b32 v31, v170, v30
	s_waitcnt lgkmcnt(0)
	v_add_f32_e32 v30, v30, v31
	ds_bpermute_b32 v31, v171, v30
	s_waitcnt lgkmcnt(0)
	v_add_f32_e32 v30, v30, v31
	ds_bpermute_b32 v31, v172, v30
	s_waitcnt lgkmcnt(0)
	v_add_f32_e32 v30, v30, v31
	ds_bpermute_b32 v31, v173, v30
	s_waitcnt lgkmcnt(0)
	v_add_f32_e32 v30, v30, v31
	v_fmamk_f32 v30, v30, 0x3a000000, v188
	v_mul_f32_e32 v31, 0x4b800000, v30
	v_cmp_gt_f32_e32 vcc, s33, v30
	s_nop 1
	v_cndmask_b32_e32 v30, v30, v31, vcc
	v_rsq_f32_e32 v30, v30
	s_nop 0
	v_mul_f32_e32 v31, 0x45800000, v30
	v_cndmask_b32_e32 v30, v30, v31, vcc
	v_pk_mul_f32 v[34:35], v[36:37], v[30:31] op_sel_hi:[1,0]
	v_pk_mul_f32 v[32:33], v[32:33], v[30:31] op_sel_hi:[1,0]
	v_pk_mul_f32 v[36:37], v[168:169], v[30:31] op_sel_hi:[1,0]
	v_pk_mul_f32 v[128:129], v[156:157], v[30:31] op_sel_hi:[1,0]
	v_pk_mul_f32 v[120:121], v[120:121], v[30:31] op_sel_hi:[1,0]
	v_pk_mul_f32 v[122:123], v[122:123], v[30:31] op_sel_hi:[1,0]
	v_pk_mul_f32 v[26:27], v[26:27], v[30:31] op_sel_hi:[1,0]
	s_waitcnt lgkmcnt(0)
	v_pk_fma_f32 v[6:7], v[6:7], v[34:35], v[2:3]
	s_nop 0
	v_cvt_pk_fp8_f32 v124, v6, v7
	v_pk_fma_f32 v[10:11], v[10:11], v[32:33], v[14:15]
	v_pk_fma_f32 v[8:9], v[8:9], v[36:37], v[4:5]
	v_cvt_pk_fp8_f32 v125, v10, v11
	v_pk_fma_f32 v[12:13], v[12:13], v[128:129], v[16:17]
	v_cvt_pk_fp8_f32 v124, v8, v9 op_sel:[0,0,1]
	v_cvt_pk_bf16_f32 v2, v6, v7
	v_cvt_pk_fp8_f32 v125, v12, v13 op_sel:[0,0,1]
	v_cvt_pk_bf16_f32 v3, v8, v9
	v_cvt_pk_bf16_f32 v4, v10, v11
	v_cvt_pk_bf16_f32 v5, v12, v13
	global_store_dwordx4 v[28:29], v[2:5], off
	global_store_dwordx2 v[38:39], v[124:125], off
	ds_read_b128 v[2:5], v205 offset:10240
	s_nop 0
	ds_read_b128 v[6:9], v205 offset:2048
	ds_read_b128 v[10:13], v205 offset:3072
	ds_read_b128 v[14:17], v205 offset:11264
	v_pk_mul_f32 v[34:35], v[126:127], v[30:31] op_sel_hi:[1,0]
	v_mov_b32_e32 v32, 0
	v_mov_b32_e32 v33, 0
	v_pk_mul_f32 v[36:37], v[144:145], v[30:31] op_sel_hi:[1,0]
	s_waitcnt lgkmcnt(0)
; #define GAS __attribute__((address_space(1)))
; #define VM_WAIT() asm volatile("s_waitcnt vmcnt(0)" ::: "memory")
; __device__ __forceinline__ unsigned cvt_pk_bf16(float lo, float hi) { unsigned r; asm volatile("v_cvt_pk_bf16_f32 %0, %1, %2" : "=v"(r) : "v"(lo), "v"(hi)); return r; }
; template <bool X8>
; __device__ __forceinline__ void ln_router_phase(Frame& F, int layer) {
;     ...
; #pragma unroll
;                 for (int j = 0; j < 4; ++j) { const int c = 8 * lane + 512 * j;
;                     const f32x4 y0 = ys[tt][j][0] * rstd * *(const GAS f32x4*)(g1 + c) + *(const GAS f32x4*)(b1 + c), y1 = ys[tt][j][1] * rstd * *(const GAS f32x4*)(g1 + c + 4) + *(const GAS f32x4*)(b1 + c + 4);
;                     u32x4 o; o.x = cvt_pk_bf16(y0[0], y0[1]); o.y = cvt_pk_bf16(y0[2], y0[3]); o.z = cvt_pk_bf16(y1[0], y1[1]); o.w = cvt_pk_bf16(y1[2], y1[3]);
;                     *(GAS u32x4*)(X1B + token * D_MODEL + c) = o;
;                     if constexpr (X8) { u32x2 w8; int q8 = __builtin_amdgcn_cvt_pk_fp8_f32(y0[0], y0[1], 0, false); q8 = __builtin_amdgcn_cvt_pk_fp8_f32(y0[2], y0[3], q8, true); w8.x = (unsigned)q8;
;                         q8 = __builtin_amdgcn_cvt_pk_fp8_f32(y1[0], y1[1], 0, false); q8 = __builtin_amdgcn_cvt_pk_fp8_f32(y1[2], y1[3], q8, true); w8.y = (unsigned)q8;
;                         *(GAS u32x2*)(X1B8 + token * D_MODEL + c) = w8; } }
;             }
;         }
;         VM_WAIT(); __syncthreads();
;         f32x4 dacc[4];
; #pragma unroll
;         for (int nb = 0; nb < 4; ++nb) dacc[nb] = (f32x4){0.f, 0.f, 0.f, 0.f};
;         const int tt4 = w & 3, kh = w >> 2;
;         u32x4 xr[4], wq[4];
;         const GAS bf16_t* wrb = (const GAS bf16_t*)(F.ws + WS_WRB) + (size_t)layer * D_MODEL * N_EXPERTS;
; #pragma unroll
;         for (int j = 0; j < 4; ++j) { const int idx = tid + 512 * j, row = idx >> 5, c8 = idx & 31; xr[j] = *(const GAS u32x4*)(X1B + (size_t)(tok0 + row) * D_MODEL + 8 * c8); }
; #pragma unroll
;         for (int j = 0; j < 4; ++j) { const int idx = tid + 512 * j, row = idx >> 3, c8 = idx & 7; wq[j] = *(const GAS u32x4*)(wrb + (size_t)row * N_EXPERTS + 8 * c8); }
	v_pk_fma_f32 v[6:7], v[6:7], v[34:35], v[2:3]
	s_nop 0
	v_cvt_pk_fp8_f32 v32, v6, v7
	v_pk_fma_f32 v[10:11], v[10:11], v[120:121], v[14:15]
	v_pk_fma_f32 v[8:9], v[8:9], v[36:37], v[4:5]
	v_cvt_pk_fp8_f32 v33, v10, v11
	v_pk_fma_f32 v[12:13], v[12:13], v[122:123], v[16:17]
	v_cvt_pk_fp8_f32 v32, v8, v9 op_sel:[0,0,1]
	v_cvt_pk_bf16_f32 v2, v6, v7
	v_cvt_pk_fp8_f32 v33, v12, v13 op_sel:[0,0,1]
	v_cvt_pk_bf16_f32 v3, v8, v9
	v_cvt_pk_bf16_f32 v4, v10, v11
	v_cvt_pk_bf16_f32 v5, v12, v13
	global_store_dwordx4 v[28:29], v[2:5], off offset:1024
	global_store_dwordx2 v[38:39], v[32:33], off offset:512
	ds_read_b128 v[2:5], v205 offset:12288
	s_nop 0
	ds_read_b128 v[6:9], v205 offset:4096
	ds_read_b128 v[10:13], v205 offset:5120
	ds_read_b128 v[14:17], v205 offset:13312
	v_pk_mul_f32 v[34:35], v[110:111], v[30:31] op_sel_hi:[1,0]
	v_pk_mul_f32 v[110:111], v[118:119], v[30:31] op_sel_hi:[1,0]
	v_mov_b32_e32 v32, 0
	v_mov_b32_e32 v33, 0
	v_pk_mul_f32 v[36:37], v[112:113], v[30:31] op_sel_hi:[1,0]
	v_pk_mul_f32 v[112:113], v[212:213], v[30:31] op_sel_hi:[1,0]
	s_waitcnt lgkmcnt(0)
	v_pk_fma_f32 v[6:7], v[34:35], v[6:7], v[2:3]
	s_nop 0
	v_cvt_pk_fp8_f32 v32, v6, v7
	v_pk_fma_f32 v[10:11], v[110:111], v[10:11], v[14:15]
	v_pk_fma_f32 v[8:9], v[36:37], v[8:9], v[4:5]
	v_cvt_pk_fp8_f32 v33, v10, v11
	v_pk_fma_f32 v[12:13], v[112:113], v[12:13], v[16:17]
	v_cvt_pk_fp8_f32 v32, v8, v9 op_sel:[0,0,1]
	v_cvt_pk_bf16_f32 v2, v6, v7
	v_cvt_pk_fp8_f32 v33, v12, v13 op_sel:[0,0,1]
	v_cvt_pk_bf16_f32 v3, v8, v9
	v_cvt_pk_bf16_f32 v4, v10, v11
	v_cvt_pk_bf16_f32 v5, v12, v13
	global_store_dwordx4 v[28:29], v[2:5], off offset:2048
	global_store_dwordx2 v[38:39], v[32:33], off offset:1024
	ds_read_b128 v[2:5], v205 offset:14336
	s_nop 0
	ds_read_b128 v[6:9], v205 offset:6144
	ds_read_b128 v[10:13], v205 offset:7168
	ds_read_b128 v[14:17], v205 offset:15360
	v_pk_mul_f32 v[34:35], v[40:41], v[30:31] op_sel_hi:[1,0]
	v_pk_mul_f32 v[36:37], v[42:43], v[30:31] op_sel_hi:[1,0]
	v_mov_b32_e32 v32, 0
	v_mov_b32_e32 v33, 0
	v_pk_mul_f32 v[30:31], v[44:45], v[30:31] op_sel_hi:[1,0]
	s_waitcnt lgkmcnt(0)
	v_pk_fma_f32 v[4:5], v[34:35], v[8:9], v[4:5]
	v_pk_fma_f32 v[2:3], v[26:27], v[6:7], v[2:3]
	v_pk_fma_f32 v[8:9], v[36:37], v[10:11], v[14:15]
	v_cvt_pk_fp8_f32 v32, v2, v3
	v_cvt_pk_fp8_f32 v33, v8, v9
	v_pk_fma_f32 v[6:7], v[30:31], v[12:13], v[16:17]
	v_cvt_pk_bf16_f32 v2, v2, v3
	v_cvt_pk_fp8_f32 v32, v4, v5 op_sel:[0,0,1]
	v_cvt_pk_fp8_f32 v33, v6, v7 op_sel:[0,0,1]
	v_cvt_pk_bf16_f32 v3, v4, v5
	v_cvt_pk_bf16_f32 v4, v8, v9
	v_cvt_pk_bf16_f32 v5, v6, v7
	global_store_dwordx4 v[28:29], v[2:5], off offset:3072
	global_store_dwordx2 v[38:39], v[32:33], off offset:1536
	s_cbranch_scc0 .LBB0_2873
	s_lshl_b32 s82, s2, 6
	v_add_u32_e32 v2, s82, v177
	v_add_u32_e32 v4, s82, v178
	v_add_u32_e32 v10, s82, v179
	v_add_u32_e32 v12, s82, v180
	v_ashrrev_i32_e32 v3, 31, v2
	v_ashrrev_i32_e32 v5, 31, v4
	v_ashrrev_i32_e32 v11, 31, v10
	v_ashrrev_i32_e32 v13, 31, v12
	v_lshlrev_b64 v[2:3], 12, v[2:3]
	v_lshlrev_b64 v[4:5], 12, v[4:5]
	v_lshlrev_b64 v[10:11], 12, v[10:11]
	v_lshlrev_b64 v[12:13], 12, v[12:13]
	v_lshl_add_u64 v[2:3], v[56:57], 0, v[2:3]
	v_lshl_add_u64 v[6:7], v[56:57], 0, v[4:5]
	v_lshl_add_u64 v[10:11], v[56:57], 0, v[10:11]
	v_lshl_add_u64 v[14:15], v[56:57], 0, v[12:13]
	s_waitcnt vmcnt(0)
	s_barrier
	global_load_dwordx4 v[2:5], v[2:3], off
	s_nop 0
	global_load_dwordx4 v[6:9], v[6:7], off
	s_nop 0
	global_load_dwordx4 v[10:13], v[10:11], off
	s_nop 0
	global_load_dwordx4 v[14:17], v[14:15], off
	s_nop 0
	global_load_dwordx4 v[18:21], v[84:85], off
	global_load_dwordx4 v[22:25], v[86:87], off
	global_load_dwordx4 v[26:29], v[88:89], off
	global_load_dwordx4 v[30:33], v[90:91], off
	v_ashrrev_i32_e32 v103, 31, v102
	v_lshlrev_b64 v[34:35], 12, v[102:103]
	v_ashrrev_i32_e32 v105, 31, v104
	v_lshl_add_u64 v[110:111], v[54:55], 0, v[34:35]
	v_lshlrev_b64 v[34:35], 12, v[104:105]
	v_ashrrev_i32_e32 v107, 31, v106
	v_lshl_add_u64 v[112:113], v[54:55], 0, v[34:35]
	v_lshlrev_b64 v[34:35], 12, v[106:107]
	v_ashrrev_i32_e32 v109, 31, v108
	v_lshl_add_u64 v[114:115], v[54:55], 0, v[34:35]
	v_lshlrev_b64 v[34:35], 12, v[108:109]
	v_lshl_add_u64 v[116:117], v[54:55], 0, v[34:35]
	v_mov_b32_e32 v34, 0
	s_mov_b32 s20, 8
	v_mov_b64_e32 v[118:119], v[100:101]
	v_mov_b64_e32 v[120:121], v[98:99]
	v_mov_b64_e32 v[122:123], v[96:97]
	v_mov_b64_e32 v[124:125], v[94:95]
	v_mov_b32_e32 v35, v34
	v_mov_b32_e32 v36, v34
	v_mov_b32_e32 v37, v34
	v_mov_b32_e32 v42, v34
	v_mov_b32_e32 v43, v34
	v_mov_b32_e32 v44, v34
	v_mov_b32_e32 v45, v34
	v_mov_b32_e32 v46, v34
	v_mov_b32_e32 v47, v34
	v_mov_b32_e32 v48, v34
	v_mov_b32_e32 v49, v34
	v_mov_b32_e32 v38, v34
	v_mov_b32_e32 v39, v34
	v_mov_b32_e32 v40, v34
	v_mov_b32_e32 v41, v34
	s_branch .LBB0_2876
